# v045 + QKV tile epilogue: q/k-norm gain vectors loaded once per tile into dead registers instead of 16 load+drain steps (epilogue de-serialisation)
# speedup vs baseline: 1.0078x; 1.0078x over previous
.LBB0_121:
	s_ashr_i32 s63, s62, 31
	s_lshl_b64 s[0:1], s[62:63], 18
	s_add_u32 s64, s9, s0
	s_addc_u32 s65, s12, s1
	s_and_b64 s[0:1], s[40:41], exec
	s_cselect_b32 s45, s65, s47
	s_cselect_b32 s44, s64, s46
	s_ashr_i32 s61, s60, 31
	s_lshl_b64 s[0:1], s[60:61], 18
	s_add_u32 s66, s13, s0
	s_addc_u32 s67, s14, s1
	ds_read_b128 v[90:93], v232
	ds_read_b128 v[94:97], v232 offset:1024
	ds_read_b128 v[98:101], v232 offset:2048
	ds_read_b128 v[102:105], v232 offset:3072
	s_and_b64 s[0:1], s[40:41], exec
	s_cselect_b32 s43, s67, s69
	s_cselect_b32 s42, s66, s68
	s_add_u32 s4, s46, 0x100
	s_addc_u32 s5, s47, 0
	s_add_u32 s6, s68, 0x100
	s_addc_u32 s7, s69, 0
	s_add_u32 s0, s46, 0x180
	s_addc_u32 s1, s47, 0
	s_add_u32 s74, s46, 0x20080
	s_addc_u32 s75, s47, 0
	v_mov_b32_e32 v2, v229
	s_add_i32 s61, s15, 0xc000
	ds_read_b128 v[38:41], v231
	ds_read_b128 v[42:45], v231 offset:1024
	ds_read_b128 v[46:49], v231 offset:2048
	ds_read_b128 v[50:53], v231 offset:3072
	ds_read_b128 v[54:57], v231 offset:4096
	ds_read_b128 v[58:61], v231 offset:5120
	ds_read_b128 v[62:65], v231 offset:6144
	s_waitcnt vmcnt(16)
	ds_read_b128 v[66:69], v231 offset:7168
	s_mov_b32 m0, s61
	s_nop 0
	global_load_lds_dwordx4 v2, s[74:75]
	s_add_u32 s74, s46, 0x30080
	s_addc_u32 s75, s47, 0
	s_add_i32 s23, s15, 0xe000
	v_mov_b32_e32 v2, v229
	s_mov_b32 m0, s23
	s_nop 0
	global_load_lds_dwordx4 v2, s[74:75]
	s_waitcnt lgkmcnt(8)
	s_barrier
	s_waitcnt lgkmcnt(0)
	s_setprio 1
	s_waitcnt lgkmcnt(0)
	v_mfma_f32_16x16x128_f8f6f4 v[2:5], v[90:97], v[38:45], 0
	v_mfma_f32_16x16x128_f8f6f4 v[6:9], v[98:105], v[38:45], 0
	v_mfma_f32_16x16x128_f8f6f4 v[10:13], v[90:97], v[46:53], 0
	v_mfma_f32_16x16x128_f8f6f4 v[14:17], v[98:105], v[46:53], 0
	v_mfma_f32_16x16x128_f8f6f4 v[18:21], v[90:97], v[54:61], 0
	v_mfma_f32_16x16x128_f8f6f4 v[22:25], v[98:105], v[54:61], 0
	v_mfma_f32_16x16x128_f8f6f4 v[26:29], v[90:97], v[62:69], 0
	v_mfma_f32_16x16x128_f8f6f4 v[30:33], v[98:105], v[62:69], 0
	s_setprio 0
	s_barrier
	v_mov_b32_e32 v34, v230
	s_mov_b32 m0, s16
	ds_read_b128 v[122:125], v232 offset:16384
	ds_read_b128 v[126:129], v232 offset:17408
	ds_read_b128 v[130:133], v232 offset:18432
	ds_read_b128 v[134:137], v232 offset:19456
	s_nop 0
	global_load_lds_dwordx4 v34, s[6:7]
	s_add_u32 s6, s68, 0x20100
	s_addc_u32 s7, s69, 0
	v_mov_b32_e32 v34, v230
	s_mov_b32 m0, s17
	s_nop 0
	global_load_lds_dwordx4 v34, s[6:7]
	s_barrier
	s_waitcnt lgkmcnt(0)
	s_setprio 1
	s_waitcnt lgkmcnt(0)
	v_mfma_f32_16x16x128_f8f6f4 v[34:37], v[122:129], v[38:45], 0
	v_mfma_f32_16x16x128_f8f6f4 v[38:41], v[130:137], v[38:45], 0
	v_mfma_f32_16x16x128_f8f6f4 v[42:45], v[122:129], v[46:53], 0
	v_mfma_f32_16x16x128_f8f6f4 v[46:49], v[130:137], v[46:53], 0
	v_mfma_f32_16x16x128_f8f6f4 v[50:53], v[122:129], v[54:61], 0
	v_mfma_f32_16x16x128_f8f6f4 v[54:57], v[130:137], v[54:61], 0
	v_mfma_f32_16x16x128_f8f6f4 v[58:61], v[122:129], v[62:69], 0
	v_mfma_f32_16x16x128_f8f6f4 v[62:65], v[130:137], v[62:69], 0
	s_setprio 0
	v_mov_b32_e32 v66, v229
	s_mov_b32 m0, s15
	s_barrier
	ds_read_b128 v[106:109], v231 offset:16384
	ds_read_b128 v[110:113], v231 offset:17408
	ds_read_b128 v[114:117], v231 offset:18432
	ds_read_b128 v[118:121], v231 offset:19456
	ds_read_b128 v[138:141], v231 offset:20480
	ds_read_b128 v[142:145], v231 offset:21504
	ds_read_b128 v[146:149], v231 offset:22528
	ds_read_b128 v[150:153], v231 offset:23552
	s_nop 0
	global_load_lds_dwordx4 v66, s[4:5]
	s_add_u32 s4, s46, 0x10100
	s_addc_u32 s5, s47, 0
	v_mov_b32_e32 v66, v229
	s_mov_b32 m0, s24
	s_nop 0
	global_load_lds_dwordx4 v66, s[4:5]
	s_barrier
	s_waitcnt lgkmcnt(0)
	s_setprio 1
	s_waitcnt lgkmcnt(0)
	v_mfma_f32_16x16x128_f8f6f4 v[66:69], v[90:97], v[106:113], 0
	v_mfma_f32_16x16x128_f8f6f4 v[70:73], v[98:105], v[106:113], 0
	v_mfma_f32_16x16x128_f8f6f4 v[74:77], v[90:97], v[114:121], 0
	v_mfma_f32_16x16x128_f8f6f4 v[78:81], v[98:105], v[114:121], 0
	v_mfma_f32_16x16x128_f8f6f4 v[82:85], v[90:97], v[138:145], 0
	v_mfma_f32_16x16x128_f8f6f4 v[86:89], v[98:105], v[138:145], 0
	v_mfma_f32_16x16x128_f8f6f4 v[90:93], v[90:97], v[146:153], 0
	v_mfma_f32_16x16x128_f8f6f4 v[94:97], v[98:105], v[146:153], 0
	s_setprio 0
	s_barrier
	s_add_u32 s4, s68, 0x8100
	s_addc_u32 s5, s69, 0
	v_mov_b32_e32 v98, v230
	s_mov_b32 m0, s25
	s_nop 0
	global_load_lds_dwordx4 v98, s[4:5]
	s_add_u32 s4, s68, 0x28100
	s_addc_u32 s5, s69, 0
	v_mov_b32_e32 v98, v230
	s_mov_b32 m0, s26
	s_nop 0
	global_load_lds_dwordx4 v98, s[4:5]
	s_waitcnt vmcnt(6)
	s_barrier
	s_setprio 1
	v_mfma_f32_16x16x128_f8f6f4 v[98:101], v[122:129], v[106:113], 0
	v_mfma_f32_16x16x128_f8f6f4 v[102:105], v[130:137], v[106:113], 0
	v_mfma_f32_16x16x128_f8f6f4 v[106:109], v[122:129], v[114:121], 0
	v_mfma_f32_16x16x128_f8f6f4 v[110:113], v[130:137], v[114:121], 0
	v_mfma_f32_16x16x128_f8f6f4 v[114:117], v[122:129], v[138:145], 0
	v_mfma_f32_16x16x128_f8f6f4 v[118:121], v[130:137], v[138:145], 0
	v_mfma_f32_16x16x128_f8f6f4 v[122:125], v[122:129], v[146:153], 0
	v_mfma_f32_16x16x128_f8f6f4 v[126:129], v[130:137], v[146:153], 0
	s_setprio 0
	s_barrier
	ds_read_b128 v[130:133], v232 offset:32768
	ds_read_b128 v[134:137], v232 offset:33792
	ds_read_b128 v[138:141], v232 offset:34816
	ds_read_b128 v[142:145], v232 offset:35840
	s_add_u32 s4, s46, 0x20100
	s_addc_u32 s5, s47, 0
	v_mov_b32_e32 v178, v229
	s_mov_b32 m0, s27
	ds_read_b128 v[146:149], v231 offset:32768
	ds_read_b128 v[150:153], v231 offset:33792
	ds_read_b128 v[154:157], v231 offset:34816
	ds_read_b128 v[158:161], v231 offset:35840
	ds_read_b128 v[162:165], v231 offset:36864
	ds_read_b128 v[166:169], v231 offset:37888
	ds_read_b128 v[170:173], v231 offset:38912
	ds_read_b128 v[174:177], v231 offset:39936
	s_nop 0
	global_load_lds_dwordx4 v178, s[4:5]
	s_add_u32 s4, s46, 0x30100
	s_addc_u32 s5, s47, 0
	v_mov_b32_e32 v178, v229
	s_mov_b32 m0, s29
	s_nop 0
	global_load_lds_dwordx4 v178, s[4:5]
	s_waitcnt lgkmcnt(8)
	s_barrier
	s_waitcnt lgkmcnt(0)
	s_setprio 1
	s_waitcnt lgkmcnt(0)
	v_mfma_f32_16x16x128_f8f6f4 v[2:5], v[130:137], v[146:153], v[2:5]
	v_mfma_f32_16x16x128_f8f6f4 v[6:9], v[138:145], v[146:153], v[6:9]
	v_mfma_f32_16x16x128_f8f6f4 v[10:13], v[130:137], v[154:161], v[10:13]
	v_mfma_f32_16x16x128_f8f6f4 v[14:17], v[138:145], v[154:161], v[14:17]
	v_mfma_f32_16x16x128_f8f6f4 v[18:21], v[130:137], v[162:169], v[18:21]
	v_mfma_f32_16x16x128_f8f6f4 v[22:25], v[138:145], v[162:169], v[22:25]
	v_mfma_f32_16x16x128_f8f6f4 v[26:29], v[130:137], v[170:177], v[26:29]
	v_mfma_f32_16x16x128_f8f6f4 v[30:33], v[138:145], v[170:177], v[30:33]
	s_setprio 0
	s_barrier
	s_add_u32 s4, s68, 0x180
	s_addc_u32 s5, s69, 0
	v_mov_b32_e32 v194, v230
	s_mov_b32 m0, s35
	ds_read_b128 v[178:181], v232 offset:49152
	ds_read_b128 v[182:185], v232 offset:50176
	ds_read_b128 v[186:189], v232 offset:51200
	ds_read_b128 v[190:193], v232 offset:52224
	s_nop 0
	global_load_lds_dwordx4 v194, s[4:5]
	s_add_u32 s4, s68, 0x20180
	s_addc_u32 s5, s69, 0
	v_mov_b32_e32 v194, v230
	s_mov_b32 m0, s36
	s_nop 0
	global_load_lds_dwordx4 v194, s[4:5]
	s_barrier
	s_waitcnt lgkmcnt(0)
	s_setprio 1
	s_waitcnt lgkmcnt(0)
	v_mfma_f32_16x16x128_f8f6f4 v[34:37], v[178:185], v[146:153], v[34:37]
	v_mfma_f32_16x16x128_f8f6f4 v[38:41], v[186:193], v[146:153], v[38:41]
	v_mfma_f32_16x16x128_f8f6f4 v[42:45], v[178:185], v[154:161], v[42:45]
	v_mfma_f32_16x16x128_f8f6f4 v[46:49], v[186:193], v[154:161], v[46:49]
	v_mfma_f32_16x16x128_f8f6f4 v[50:53], v[178:185], v[162:169], v[50:53]
	v_mfma_f32_16x16x128_f8f6f4 v[54:57], v[186:193], v[162:169], v[54:57]
	v_mfma_f32_16x16x128_f8f6f4 v[58:61], v[178:185], v[170:177], v[58:61]
	v_mfma_f32_16x16x128_f8f6f4 v[62:65], v[186:193], v[170:177], v[62:65]
	s_setprio 0
	v_mov_b32_e32 v194, v229
	s_mov_b32 m0, s37
	s_barrier
	ds_read_b128 v[146:149], v231 offset:49152
	ds_read_b128 v[150:153], v231 offset:50176
	ds_read_b128 v[154:157], v231 offset:51200
	ds_read_b128 v[158:161], v231 offset:52224
	ds_read_b128 v[162:165], v231 offset:53248
	ds_read_b128 v[166:169], v231 offset:54272
	ds_read_b128 v[170:173], v231 offset:55296
	ds_read_b128 v[174:177], v231 offset:56320
	s_nop 0
	global_load_lds_dwordx4 v194, s[0:1]
	s_add_u32 s0, s46, 0x10180
	s_addc_u32 s1, s47, 0
	v_mov_b32_e32 v194, v229
	s_mov_b32 m0, s70
	s_nop 0
	global_load_lds_dwordx4 v194, s[0:1]
	s_barrier
	s_waitcnt lgkmcnt(0)
	s_setprio 1
	s_waitcnt lgkmcnt(0)
	v_mfma_f32_16x16x128_f8f6f4 v[70:73], v[138:145], v[146:153], v[70:73]
	v_mfma_f32_16x16x128_f8f6f4 v[74:77], v[130:137], v[154:161], v[74:77]
	v_mfma_f32_16x16x128_f8f6f4 v[78:81], v[138:145], v[154:161], v[78:81]
	v_mfma_f32_16x16x128_f8f6f4 v[82:85], v[130:137], v[162:169], v[82:85]
	v_mfma_f32_16x16x128_f8f6f4 v[86:89], v[138:145], v[162:169], v[86:89]
	v_mfma_f32_16x16x128_f8f6f4 v[90:93], v[130:137], v[170:177], v[90:93]
	v_mfma_f32_16x16x128_f8f6f4 v[94:97], v[138:145], v[170:177], v[94:97]
	v_mfma_f32_16x16x128_f8f6f4 v[66:69], v[130:137], v[146:153], v[66:69]
	s_setprio 0
	s_barrier
	s_add_u32 s0, s68, 0x8180
	s_addc_u32 s1, s69, 0
	v_mov_b32_e32 v130, v230
	s_mov_b32 m0, s71
	s_nop 0
	global_load_lds_dwordx4 v130, s[0:1]
	s_add_u32 s0, s68, 0x28180
	s_addc_u32 s1, s69, 0
	v_mov_b32_e32 v130, v230
	s_mov_b32 m0, s72
	s_nop 0
	global_load_lds_dwordx4 v130, s[0:1]
	s_waitcnt vmcnt(6)
	s_barrier
	s_setprio 1
	v_mfma_f32_16x16x128_f8f6f4 v[98:101], v[178:185], v[146:153], v[98:101]
	v_mfma_f32_16x16x128_f8f6f4 v[102:105], v[186:193], v[146:153], v[102:105]
	v_mfma_f32_16x16x128_f8f6f4 v[106:109], v[178:185], v[154:161], v[106:109]
	v_mfma_f32_16x16x128_f8f6f4 v[110:113], v[186:193], v[154:161], v[110:113]
	v_mfma_f32_16x16x128_f8f6f4 v[114:117], v[178:185], v[162:169], v[114:117]
	v_mfma_f32_16x16x128_f8f6f4 v[118:121], v[186:193], v[162:169], v[118:121]
	v_mfma_f32_16x16x128_f8f6f4 v[122:125], v[178:185], v[170:177], v[122:125]
	v_mfma_f32_16x16x128_f8f6f4 v[126:129], v[186:193], v[170:177], v[126:129]
	s_setprio 0
	s_barrier
	ds_read_b128 v[130:133], v232
	ds_read_b128 v[134:137], v232 offset:1024
	ds_read_b128 v[138:141], v232 offset:2048
	ds_read_b128 v[142:145], v232 offset:3072
	s_add_u32 s4, s46, 0x200
	s_addc_u32 s5, s47, 0
	s_add_u32 s6, s68, 0x200
	s_addc_u32 s7, s69, 0
	s_add_u32 s0, s46, 0x280
	s_addc_u32 s1, s47, 0
	s_add_u32 s74, s46, 0x20180
	s_addc_u32 s75, s47, 0
	v_mov_b32_e32 v178, v229
	s_mov_b32 m0, s61
	ds_read_b128 v[146:149], v231
	ds_read_b128 v[150:153], v231 offset:1024
	ds_read_b128 v[154:157], v231 offset:2048
	ds_read_b128 v[158:161], v231 offset:3072
	ds_read_b128 v[162:165], v231 offset:4096
	ds_read_b128 v[166:169], v231 offset:5120
	ds_read_b128 v[170:173], v231 offset:6144
	ds_read_b128 v[174:177], v231 offset:7168
	s_nop 0
	global_load_lds_dwordx4 v178, s[74:75]
	s_add_u32 s74, s46, 0x30180
	s_addc_u32 s75, s47, 0
	v_mov_b32_e32 v178, v229
	s_mov_b32 m0, s23
	s_nop 0
	global_load_lds_dwordx4 v178, s[74:75]
	s_waitcnt lgkmcnt(8)
	s_barrier
	s_waitcnt lgkmcnt(0)
	s_setprio 1
	s_waitcnt lgkmcnt(0)
	v_mfma_f32_16x16x128_f8f6f4 v[2:5], v[130:137], v[146:153], v[2:5]
	v_mfma_f32_16x16x128_f8f6f4 v[6:9], v[138:145], v[146:153], v[6:9]
	v_mfma_f32_16x16x128_f8f6f4 v[10:13], v[130:137], v[154:161], v[10:13]
	v_mfma_f32_16x16x128_f8f6f4 v[14:17], v[138:145], v[154:161], v[14:17]
	v_mfma_f32_16x16x128_f8f6f4 v[18:21], v[130:137], v[162:169], v[18:21]
	v_mfma_f32_16x16x128_f8f6f4 v[22:25], v[138:145], v[162:169], v[22:25]
	v_mfma_f32_16x16x128_f8f6f4 v[26:29], v[130:137], v[170:177], v[26:29]
	v_mfma_f32_16x16x128_f8f6f4 v[30:33], v[138:145], v[170:177], v[30:33]
	s_setprio 0
	s_barrier
	v_mov_b32_e32 v194, v230
	s_mov_b32 m0, s16
	ds_read_b128 v[178:181], v232 offset:16384
	ds_read_b128 v[182:185], v232 offset:17408
	ds_read_b128 v[186:189], v232 offset:18432
	ds_read_b128 v[190:193], v232 offset:19456
	s_nop 0
	global_load_lds_dwordx4 v194, s[6:7]
	s_add_u32 s6, s68, 0x20200
	s_addc_u32 s7, s69, 0
	v_mov_b32_e32 v194, v230
	s_mov_b32 m0, s17
	s_nop 0
	global_load_lds_dwordx4 v194, s[6:7]
	s_barrier
	s_waitcnt lgkmcnt(0)
	s_setprio 1
	s_waitcnt lgkmcnt(0)
	v_mfma_f32_16x16x128_f8f6f4 v[34:37], v[178:185], v[146:153], v[34:37]
	v_mfma_f32_16x16x128_f8f6f4 v[38:41], v[186:193], v[146:153], v[38:41]
	v_mfma_f32_16x16x128_f8f6f4 v[42:45], v[178:185], v[154:161], v[42:45]
	v_mfma_f32_16x16x128_f8f6f4 v[46:49], v[186:193], v[154:161], v[46:49]
	v_mfma_f32_16x16x128_f8f6f4 v[50:53], v[178:185], v[162:169], v[50:53]
	v_mfma_f32_16x16x128_f8f6f4 v[54:57], v[186:193], v[162:169], v[54:57]
	v_mfma_f32_16x16x128_f8f6f4 v[58:61], v[178:185], v[170:177], v[58:61]
	v_mfma_f32_16x16x128_f8f6f4 v[62:65], v[186:193], v[170:177], v[62:65]
	s_setprio 0
	v_mov_b32_e32 v194, v229
	s_mov_b32 m0, s15
	s_barrier
	ds_read_b128 v[146:149], v231 offset:16384
	ds_read_b128 v[150:153], v231 offset:17408
	ds_read_b128 v[154:157], v231 offset:18432
	ds_read_b128 v[158:161], v231 offset:19456
	ds_read_b128 v[162:165], v231 offset:20480
	ds_read_b128 v[166:169], v231 offset:21504
	ds_read_b128 v[170:173], v231 offset:22528
	ds_read_b128 v[174:177], v231 offset:23552
	s_nop 0
	global_load_lds_dwordx4 v194, s[4:5]
	s_add_u32 s4, s46, 0x10200
	s_addc_u32 s5, s47, 0
	v_mov_b32_e32 v194, v229
	s_mov_b32 m0, s24
	s_nop 0
	global_load_lds_dwordx4 v194, s[4:5]
	s_barrier
	s_waitcnt lgkmcnt(0)
	s_setprio 1
	s_waitcnt lgkmcnt(0)
	v_mfma_f32_16x16x128_f8f6f4 v[70:73], v[138:145], v[146:153], v[70:73]
	v_mfma_f32_16x16x128_f8f6f4 v[74:77], v[130:137], v[154:161], v[74:77]
	v_mfma_f32_16x16x128_f8f6f4 v[78:81], v[138:145], v[154:161], v[78:81]
	v_mfma_f32_16x16x128_f8f6f4 v[82:85], v[130:137], v[162:169], v[82:85]
	v_mfma_f32_16x16x128_f8f6f4 v[86:89], v[138:145], v[162:169], v[86:89]
	v_mfma_f32_16x16x128_f8f6f4 v[90:93], v[130:137], v[170:177], v[90:93]
	v_mfma_f32_16x16x128_f8f6f4 v[94:97], v[138:145], v[170:177], v[94:97]
	v_mfma_f32_16x16x128_f8f6f4 v[66:69], v[130:137], v[146:153], v[66:69]
	s_setprio 0
	s_barrier
	s_add_u32 s4, s68, 0x8200
	s_addc_u32 s5, s69, 0
	v_mov_b32_e32 v130, v230
	s_mov_b32 m0, s25
	s_nop 0
	global_load_lds_dwordx4 v130, s[4:5]
	s_add_u32 s4, s68, 0x28200
	s_addc_u32 s5, s69, 0
	v_mov_b32_e32 v130, v230
	s_mov_b32 m0, s26
	s_nop 0
	global_load_lds_dwordx4 v130, s[4:5]
	s_waitcnt vmcnt(6)
	s_barrier
	s_setprio 1
	v_mfma_f32_16x16x128_f8f6f4 v[98:101], v[178:185], v[146:153], v[98:101]
	v_mfma_f32_16x16x128_f8f6f4 v[102:105], v[186:193], v[146:153], v[102:105]
	v_mfma_f32_16x16x128_f8f6f4 v[106:109], v[178:185], v[154:161], v[106:109]
	v_mfma_f32_16x16x128_f8f6f4 v[110:113], v[186:193], v[154:161], v[110:113]
	v_mfma_f32_16x16x128_f8f6f4 v[114:117], v[178:185], v[162:169], v[114:117]
	v_mfma_f32_16x16x128_f8f6f4 v[118:121], v[186:193], v[162:169], v[118:121]
	v_mfma_f32_16x16x128_f8f6f4 v[122:125], v[178:185], v[170:177], v[122:125]
	v_mfma_f32_16x16x128_f8f6f4 v[126:129], v[186:193], v[170:177], v[126:129]
	s_setprio 0
	s_barrier
	ds_read_b128 v[130:133], v232 offset:32768
	ds_read_b128 v[134:137], v232 offset:33792
	ds_read_b128 v[138:141], v232 offset:34816
	ds_read_b128 v[142:145], v232 offset:35840
	s_add_u32 s4, s46, 0x20200
	s_addc_u32 s5, s47, 0
	v_mov_b32_e32 v178, v229
	s_mov_b32 m0, s27
	ds_read_b128 v[146:149], v231 offset:32768
	ds_read_b128 v[150:153], v231 offset:33792
	ds_read_b128 v[154:157], v231 offset:34816
	ds_read_b128 v[158:161], v231 offset:35840
	ds_read_b128 v[162:165], v231 offset:36864
	ds_read_b128 v[166:169], v231 offset:37888
	ds_read_b128 v[170:173], v231 offset:38912
	ds_read_b128 v[174:177], v231 offset:39936
	s_nop 0
	global_load_lds_dwordx4 v178, s[4:5]
	s_add_u32 s4, s46, 0x30200
	s_addc_u32 s5, s47, 0
	v_mov_b32_e32 v178, v229
	s_mov_b32 m0, s29
	s_nop 0
	global_load_lds_dwordx4 v178, s[4:5]
	s_waitcnt lgkmcnt(8)
	s_barrier
	s_waitcnt lgkmcnt(0)
	s_setprio 1
	s_waitcnt lgkmcnt(0)
	v_mfma_f32_16x16x128_f8f6f4 v[2:5], v[130:137], v[146:153], v[2:5]
	v_mfma_f32_16x16x128_f8f6f4 v[6:9], v[138:145], v[146:153], v[6:9]
	v_mfma_f32_16x16x128_f8f6f4 v[10:13], v[130:137], v[154:161], v[10:13]
	v_mfma_f32_16x16x128_f8f6f4 v[14:17], v[138:145], v[154:161], v[14:17]
	v_mfma_f32_16x16x128_f8f6f4 v[18:21], v[130:137], v[162:169], v[18:21]
	v_mfma_f32_16x16x128_f8f6f4 v[22:25], v[138:145], v[162:169], v[22:25]
	v_mfma_f32_16x16x128_f8f6f4 v[26:29], v[130:137], v[170:177], v[26:29]
	v_mfma_f32_16x16x128_f8f6f4 v[30:33], v[138:145], v[170:177], v[30:33]
	s_setprio 0
	s_barrier
	s_add_u32 s4, s68, 0x280
	s_addc_u32 s5, s69, 0
	v_mov_b32_e32 v194, v230
	s_mov_b32 m0, s35
	ds_read_b128 v[178:181], v232 offset:49152
	ds_read_b128 v[182:185], v232 offset:50176
	ds_read_b128 v[186:189], v232 offset:51200
	ds_read_b128 v[190:193], v232 offset:52224
	s_nop 0
	global_load_lds_dwordx4 v194, s[4:5]
	s_add_u32 s4, s68, 0x20280
	s_addc_u32 s5, s69, 0
	v_mov_b32_e32 v194, v230
	s_mov_b32 m0, s36
	s_nop 0
	global_load_lds_dwordx4 v194, s[4:5]
	s_barrier
	s_waitcnt lgkmcnt(0)
	s_setprio 1
	s_waitcnt lgkmcnt(0)
	v_mfma_f32_16x16x128_f8f6f4 v[34:37], v[178:185], v[146:153], v[34:37]
	v_mfma_f32_16x16x128_f8f6f4 v[38:41], v[186:193], v[146:153], v[38:41]
	v_mfma_f32_16x16x128_f8f6f4 v[42:45], v[178:185], v[154:161], v[42:45]
	v_mfma_f32_16x16x128_f8f6f4 v[46:49], v[186:193], v[154:161], v[46:49]
	v_mfma_f32_16x16x128_f8f6f4 v[50:53], v[178:185], v[162:169], v[50:53]
	v_mfma_f32_16x16x128_f8f6f4 v[54:57], v[186:193], v[162:169], v[54:57]
	v_mfma_f32_16x16x128_f8f6f4 v[58:61], v[178:185], v[170:177], v[58:61]
	v_mfma_f32_16x16x128_f8f6f4 v[62:65], v[186:193], v[170:177], v[62:65]
	s_setprio 0
	v_mov_b32_e32 v194, v229
	s_mov_b32 m0, s37
	s_barrier
	ds_read_b128 v[146:149], v231 offset:49152
	ds_read_b128 v[150:153], v231 offset:50176
	ds_read_b128 v[154:157], v231 offset:51200
	ds_read_b128 v[158:161], v231 offset:52224
	ds_read_b128 v[162:165], v231 offset:53248
	ds_read_b128 v[166:169], v231 offset:54272
	ds_read_b128 v[170:173], v231 offset:55296
	ds_read_b128 v[174:177], v231 offset:56320
	s_nop 0
	global_load_lds_dwordx4 v194, s[0:1]
	s_add_u32 s0, s46, 0x10280
	s_addc_u32 s1, s47, 0
	v_mov_b32_e32 v194, v229
	s_mov_b32 m0, s70
	s_nop 0
	global_load_lds_dwordx4 v194, s[0:1]
	s_barrier
	s_waitcnt lgkmcnt(0)
	s_setprio 1
	s_waitcnt lgkmcnt(0)
	v_mfma_f32_16x16x128_f8f6f4 v[70:73], v[138:145], v[146:153], v[70:73]
	v_mfma_f32_16x16x128_f8f6f4 v[74:77], v[130:137], v[154:161], v[74:77]
	v_mfma_f32_16x16x128_f8f6f4 v[78:81], v[138:145], v[154:161], v[78:81]
	v_mfma_f32_16x16x128_f8f6f4 v[82:85], v[130:137], v[162:169], v[82:85]
	v_mfma_f32_16x16x128_f8f6f4 v[86:89], v[138:145], v[162:169], v[86:89]
	v_mfma_f32_16x16x128_f8f6f4 v[90:93], v[130:137], v[170:177], v[90:93]
	v_mfma_f32_16x16x128_f8f6f4 v[94:97], v[138:145], v[170:177], v[94:97]
	v_mfma_f32_16x16x128_f8f6f4 v[66:69], v[130:137], v[146:153], v[66:69]
	s_setprio 0
	s_barrier
	s_add_u32 s0, s68, 0x8280
	s_addc_u32 s1, s69, 0
	v_mov_b32_e32 v130, v230
	s_mov_b32 m0, s71
	s_nop 0
	global_load_lds_dwordx4 v130, s[0:1]
	s_add_u32 s0, s68, 0x28280
	s_addc_u32 s1, s69, 0
	v_mov_b32_e32 v130, v230
	s_mov_b32 m0, s72
	s_nop 0
	global_load_lds_dwordx4 v130, s[0:1]
	s_waitcnt vmcnt(6)
	s_barrier
	s_setprio 1
	v_mfma_f32_16x16x128_f8f6f4 v[98:101], v[178:185], v[146:153], v[98:101]
	v_mfma_f32_16x16x128_f8f6f4 v[102:105], v[186:193], v[146:153], v[102:105]
	v_mfma_f32_16x16x128_f8f6f4 v[106:109], v[178:185], v[154:161], v[106:109]
	v_mfma_f32_16x16x128_f8f6f4 v[110:113], v[186:193], v[154:161], v[110:113]
	v_mfma_f32_16x16x128_f8f6f4 v[114:117], v[178:185], v[162:169], v[114:117]
	v_mfma_f32_16x16x128_f8f6f4 v[118:121], v[186:193], v[162:169], v[118:121]
	v_mfma_f32_16x16x128_f8f6f4 v[122:125], v[178:185], v[170:177], v[122:125]
	v_mfma_f32_16x16x128_f8f6f4 v[126:129], v[186:193], v[170:177], v[126:129]
	s_setprio 0
	s_barrier
	ds_read_b128 v[130:133], v232
	ds_read_b128 v[134:137], v232 offset:1024
	ds_read_b128 v[138:141], v232 offset:2048
	ds_read_b128 v[142:145], v232 offset:3072
	s_add_u32 s4, s46, 0x300
	s_addc_u32 s5, s47, 0
	s_add_u32 s6, s68, 0x300
	s_addc_u32 s7, s69, 0
	s_add_u32 s0, s46, 0x380
	s_addc_u32 s1, s47, 0
	s_add_u32 s74, s46, 0x20280
	s_addc_u32 s75, s47, 0
	v_mov_b32_e32 v178, v229
	s_mov_b32 m0, s61
	ds_read_b128 v[146:149], v231
	ds_read_b128 v[150:153], v231 offset:1024
	ds_read_b128 v[154:157], v231 offset:2048
	ds_read_b128 v[158:161], v231 offset:3072
	ds_read_b128 v[162:165], v231 offset:4096
	ds_read_b128 v[166:169], v231 offset:5120
	ds_read_b128 v[170:173], v231 offset:6144
	ds_read_b128 v[174:177], v231 offset:7168
	s_nop 0
	global_load_lds_dwordx4 v178, s[74:75]
	s_add_u32 s74, s46, 0x30280
	s_addc_u32 s75, s47, 0
	v_mov_b32_e32 v178, v229
	s_mov_b32 m0, s23
	s_nop 0
	global_load_lds_dwordx4 v178, s[74:75]
	s_waitcnt lgkmcnt(8)
	s_barrier
	s_waitcnt lgkmcnt(0)
	s_setprio 1
	s_waitcnt lgkmcnt(0)
	v_mfma_f32_16x16x128_f8f6f4 v[2:5], v[130:137], v[146:153], v[2:5]
	v_mfma_f32_16x16x128_f8f6f4 v[6:9], v[138:145], v[146:153], v[6:9]
	v_mfma_f32_16x16x128_f8f6f4 v[10:13], v[130:137], v[154:161], v[10:13]
	v_mfma_f32_16x16x128_f8f6f4 v[14:17], v[138:145], v[154:161], v[14:17]
	v_mfma_f32_16x16x128_f8f6f4 v[18:21], v[130:137], v[162:169], v[18:21]
	v_mfma_f32_16x16x128_f8f6f4 v[22:25], v[138:145], v[162:169], v[22:25]
	v_mfma_f32_16x16x128_f8f6f4 v[26:29], v[130:137], v[170:177], v[26:29]
	v_mfma_f32_16x16x128_f8f6f4 v[30:33], v[138:145], v[170:177], v[30:33]
	s_setprio 0
	s_barrier
	v_mov_b32_e32 v194, v230
	s_mov_b32 m0, s16
	ds_read_b128 v[178:181], v232 offset:16384
	ds_read_b128 v[182:185], v232 offset:17408
	ds_read_b128 v[186:189], v232 offset:18432
	ds_read_b128 v[190:193], v232 offset:19456
	s_nop 0
	global_load_lds_dwordx4 v194, s[6:7]
	s_add_u32 s6, s68, 0x20300
	s_addc_u32 s7, s69, 0
	v_mov_b32_e32 v194, v230
	s_mov_b32 m0, s17
	s_nop 0
	global_load_lds_dwordx4 v194, s[6:7]
	s_barrier
	s_waitcnt lgkmcnt(0)
	s_setprio 1
	s_waitcnt lgkmcnt(0)
	v_mfma_f32_16x16x128_f8f6f4 v[34:37], v[178:185], v[146:153], v[34:37]
	v_mfma_f32_16x16x128_f8f6f4 v[38:41], v[186:193], v[146:153], v[38:41]
	v_mfma_f32_16x16x128_f8f6f4 v[42:45], v[178:185], v[154:161], v[42:45]
	v_mfma_f32_16x16x128_f8f6f4 v[46:49], v[186:193], v[154:161], v[46:49]
	v_mfma_f32_16x16x128_f8f6f4 v[50:53], v[178:185], v[162:169], v[50:53]
	v_mfma_f32_16x16x128_f8f6f4 v[54:57], v[186:193], v[162:169], v[54:57]
	v_mfma_f32_16x16x128_f8f6f4 v[58:61], v[178:185], v[170:177], v[58:61]
	v_mfma_f32_16x16x128_f8f6f4 v[62:65], v[186:193], v[170:177], v[62:65]
	s_setprio 0
	v_mov_b32_e32 v194, v229
	s_mov_b32 m0, s15
	s_barrier
	ds_read_b128 v[146:149], v231 offset:16384
	ds_read_b128 v[150:153], v231 offset:17408
	ds_read_b128 v[154:157], v231 offset:18432
	ds_read_b128 v[158:161], v231 offset:19456
	ds_read_b128 v[162:165], v231 offset:20480
	ds_read_b128 v[166:169], v231 offset:21504
	ds_read_b128 v[170:173], v231 offset:22528
	ds_read_b128 v[174:177], v231 offset:23552
	s_nop 0
	global_load_lds_dwordx4 v194, s[4:5]
	s_add_u32 s4, s46, 0x10300
	s_addc_u32 s5, s47, 0
	v_mov_b32_e32 v194, v229
	s_mov_b32 m0, s24
	s_nop 0
	global_load_lds_dwordx4 v194, s[4:5]
	s_barrier
	s_waitcnt lgkmcnt(0)
	s_setprio 1
	s_waitcnt lgkmcnt(0)
	v_mfma_f32_16x16x128_f8f6f4 v[70:73], v[138:145], v[146:153], v[70:73]
	v_mfma_f32_16x16x128_f8f6f4 v[74:77], v[130:137], v[154:161], v[74:77]
	v_mfma_f32_16x16x128_f8f6f4 v[78:81], v[138:145], v[154:161], v[78:81]
	v_mfma_f32_16x16x128_f8f6f4 v[82:85], v[130:137], v[162:169], v[82:85]
	v_mfma_f32_16x16x128_f8f6f4 v[86:89], v[138:145], v[162:169], v[86:89]
	v_mfma_f32_16x16x128_f8f6f4 v[90:93], v[130:137], v[170:177], v[90:93]
	v_mfma_f32_16x16x128_f8f6f4 v[94:97], v[138:145], v[170:177], v[94:97]
	v_mfma_f32_16x16x128_f8f6f4 v[66:69], v[130:137], v[146:153], v[66:69]
	s_setprio 0
	s_barrier
	s_add_u32 s4, s68, 0x8300
	s_addc_u32 s5, s69, 0
	v_mov_b32_e32 v130, v230
	s_mov_b32 m0, s25
	s_nop 0
	global_load_lds_dwordx4 v130, s[4:5]
	s_add_u32 s4, s68, 0x28300
	s_addc_u32 s5, s69, 0
	v_mov_b32_e32 v130, v230
	s_mov_b32 m0, s26
	s_nop 0
	global_load_lds_dwordx4 v130, s[4:5]
	s_waitcnt vmcnt(6)
	s_barrier
	s_setprio 1
	v_mfma_f32_16x16x128_f8f6f4 v[98:101], v[178:185], v[146:153], v[98:101]
	v_mfma_f32_16x16x128_f8f6f4 v[102:105], v[186:193], v[146:153], v[102:105]
	v_mfma_f32_16x16x128_f8f6f4 v[106:109], v[178:185], v[154:161], v[106:109]
	v_mfma_f32_16x16x128_f8f6f4 v[110:113], v[186:193], v[154:161], v[110:113]
	v_mfma_f32_16x16x128_f8f6f4 v[114:117], v[178:185], v[162:169], v[114:117]
	v_mfma_f32_16x16x128_f8f6f4 v[118:121], v[186:193], v[162:169], v[118:121]
	v_mfma_f32_16x16x128_f8f6f4 v[122:125], v[178:185], v[170:177], v[122:125]
	v_mfma_f32_16x16x128_f8f6f4 v[126:129], v[186:193], v[170:177], v[126:129]
	s_setprio 0
	s_barrier
	ds_read_b128 v[130:133], v232 offset:32768
	ds_read_b128 v[134:137], v232 offset:33792
	ds_read_b128 v[138:141], v232 offset:34816
	ds_read_b128 v[142:145], v232 offset:35840
	s_add_u32 s4, s46, 0x20300
	s_addc_u32 s5, s47, 0
	v_mov_b32_e32 v178, v229
	s_mov_b32 m0, s27
	ds_read_b128 v[146:149], v231 offset:32768
	ds_read_b128 v[150:153], v231 offset:33792
	ds_read_b128 v[154:157], v231 offset:34816
	ds_read_b128 v[158:161], v231 offset:35840
	ds_read_b128 v[162:165], v231 offset:36864
	ds_read_b128 v[166:169], v231 offset:37888
	ds_read_b128 v[170:173], v231 offset:38912
	ds_read_b128 v[174:177], v231 offset:39936
	s_nop 0
	global_load_lds_dwordx4 v178, s[4:5]
	s_add_u32 s4, s46, 0x30300
	s_addc_u32 s5, s47, 0
	v_mov_b32_e32 v178, v229
	s_mov_b32 m0, s29
	s_nop 0
	global_load_lds_dwordx4 v178, s[4:5]
	s_waitcnt lgkmcnt(8)
	s_barrier
	s_waitcnt lgkmcnt(0)
	s_setprio 1
	s_waitcnt lgkmcnt(0)
	v_mfma_f32_16x16x128_f8f6f4 v[2:5], v[130:137], v[146:153], v[2:5]
	v_mfma_f32_16x16x128_f8f6f4 v[6:9], v[138:145], v[146:153], v[6:9]
	v_mfma_f32_16x16x128_f8f6f4 v[10:13], v[130:137], v[154:161], v[10:13]
	v_mfma_f32_16x16x128_f8f6f4 v[14:17], v[138:145], v[154:161], v[14:17]
	v_mfma_f32_16x16x128_f8f6f4 v[18:21], v[130:137], v[162:169], v[18:21]
	v_mfma_f32_16x16x128_f8f6f4 v[22:25], v[138:145], v[162:169], v[22:25]
	v_mfma_f32_16x16x128_f8f6f4 v[26:29], v[130:137], v[170:177], v[26:29]
	v_mfma_f32_16x16x128_f8f6f4 v[30:33], v[138:145], v[170:177], v[30:33]
	s_setprio 0
	s_barrier
	s_add_u32 s4, s68, 0x380
	s_addc_u32 s5, s69, 0
	v_mov_b32_e32 v194, v230
	s_mov_b32 m0, s35
	ds_read_b128 v[178:181], v232 offset:49152
	ds_read_b128 v[182:185], v232 offset:50176
	ds_read_b128 v[186:189], v232 offset:51200
	ds_read_b128 v[190:193], v232 offset:52224
	s_nop 0
	global_load_lds_dwordx4 v194, s[4:5]
	s_add_u32 s4, s68, 0x20380
	s_addc_u32 s5, s69, 0
	v_mov_b32_e32 v194, v230
	s_mov_b32 m0, s36
	s_nop 0
	global_load_lds_dwordx4 v194, s[4:5]
	s_barrier
	s_waitcnt lgkmcnt(0)
	s_setprio 1
	s_waitcnt lgkmcnt(0)
	v_mfma_f32_16x16x128_f8f6f4 v[34:37], v[178:185], v[146:153], v[34:37]
	v_mfma_f32_16x16x128_f8f6f4 v[38:41], v[186:193], v[146:153], v[38:41]
	v_mfma_f32_16x16x128_f8f6f4 v[42:45], v[178:185], v[154:161], v[42:45]
	v_mfma_f32_16x16x128_f8f6f4 v[46:49], v[186:193], v[154:161], v[46:49]
	v_mfma_f32_16x16x128_f8f6f4 v[50:53], v[178:185], v[162:169], v[50:53]
	v_mfma_f32_16x16x128_f8f6f4 v[54:57], v[186:193], v[162:169], v[54:57]
	v_mfma_f32_16x16x128_f8f6f4 v[58:61], v[178:185], v[170:177], v[58:61]
	v_mfma_f32_16x16x128_f8f6f4 v[62:65], v[186:193], v[170:177], v[62:65]
	s_setprio 0
	v_mov_b32_e32 v194, v229
	s_mov_b32 m0, s37
	s_barrier
	ds_read_b128 v[146:149], v231 offset:49152
	ds_read_b128 v[150:153], v231 offset:50176
	ds_read_b128 v[154:157], v231 offset:51200
	ds_read_b128 v[158:161], v231 offset:52224
	ds_read_b128 v[162:165], v231 offset:53248
	ds_read_b128 v[166:169], v231 offset:54272
	ds_read_b128 v[170:173], v231 offset:55296
	ds_read_b128 v[174:177], v231 offset:56320
	s_nop 0
	global_load_lds_dwordx4 v194, s[0:1]
	s_add_u32 s0, s46, 0x10380
	s_addc_u32 s1, s47, 0
	v_mov_b32_e32 v194, v229
	s_mov_b32 m0, s70
	s_nop 0
	global_load_lds_dwordx4 v194, s[0:1]
	s_barrier
	s_waitcnt lgkmcnt(0)
	s_setprio 1
	s_waitcnt lgkmcnt(0)
	v_mfma_f32_16x16x128_f8f6f4 v[70:73], v[138:145], v[146:153], v[70:73]
	v_mfma_f32_16x16x128_f8f6f4 v[74:77], v[130:137], v[154:161], v[74:77]
	v_mfma_f32_16x16x128_f8f6f4 v[78:81], v[138:145], v[154:161], v[78:81]
	v_mfma_f32_16x16x128_f8f6f4 v[82:85], v[130:137], v[162:169], v[82:85]
	v_mfma_f32_16x16x128_f8f6f4 v[86:89], v[138:145], v[162:169], v[86:89]
	v_mfma_f32_16x16x128_f8f6f4 v[90:93], v[130:137], v[170:177], v[90:93]
	v_mfma_f32_16x16x128_f8f6f4 v[94:97], v[138:145], v[170:177], v[94:97]
	v_mfma_f32_16x16x128_f8f6f4 v[66:69], v[130:137], v[146:153], v[66:69]
	s_setprio 0
	s_barrier
	s_add_u32 s0, s68, 0x8380
	s_addc_u32 s1, s69, 0
	v_mov_b32_e32 v130, v230
	s_mov_b32 m0, s71
	s_nop 0
	global_load_lds_dwordx4 v130, s[0:1]
	s_add_u32 s0, s68, 0x28380
	s_addc_u32 s1, s69, 0
	v_mov_b32_e32 v130, v230
	s_mov_b32 m0, s72
	s_nop 0
	global_load_lds_dwordx4 v130, s[0:1]
	s_waitcnt vmcnt(6)
	s_barrier
	s_setprio 1
	v_mfma_f32_16x16x128_f8f6f4 v[98:101], v[178:185], v[146:153], v[98:101]
	v_mfma_f32_16x16x128_f8f6f4 v[102:105], v[186:193], v[146:153], v[102:105]
	v_mfma_f32_16x16x128_f8f6f4 v[106:109], v[178:185], v[154:161], v[106:109]
	v_mfma_f32_16x16x128_f8f6f4 v[110:113], v[186:193], v[154:161], v[110:113]
	v_mfma_f32_16x16x128_f8f6f4 v[114:117], v[178:185], v[162:169], v[114:117]
	v_mfma_f32_16x16x128_f8f6f4 v[118:121], v[186:193], v[162:169], v[118:121]
	v_mfma_f32_16x16x128_f8f6f4 v[122:125], v[178:185], v[170:177], v[122:125]
	v_mfma_f32_16x16x128_f8f6f4 v[126:129], v[186:193], v[170:177], v[126:129]
	s_setprio 0
	s_barrier
	ds_read_b128 v[134:137], v232
	ds_read_b128 v[138:141], v232 offset:1024
	ds_read_b128 v[142:145], v232 offset:2048
	ds_read_b128 v[146:149], v232 offset:3072
	s_add_u32 s0, s44, 0x80
	s_addc_u32 s1, s45, 0
	s_add_u32 s4, s46, 0x20380
	s_addc_u32 s5, s47, 0
	v_mov_b32_e32 v130, v229
	s_mov_b32 m0, s61
	ds_read_b128 v[150:153], v231
	ds_read_b128 v[154:157], v231 offset:1024
	ds_read_b128 v[158:161], v231 offset:2048
	ds_read_b128 v[162:165], v231 offset:3072
	ds_read_b128 v[166:169], v231 offset:4096
	ds_read_b128 v[170:173], v231 offset:5120
	ds_read_b128 v[234:237], v231 offset:6144
	ds_read_b128 v[238:241], v231 offset:7168
	s_nop 0
	global_load_lds_dwordx4 v130, s[4:5]
	s_add_u32 s4, s46, 0x30380
	s_addc_u32 s5, s47, 0
	v_mov_b32_e32 v130, v229
	s_mov_b32 m0, s23
	s_nop 0
	global_load_lds_dwordx4 v130, s[4:5]
	s_waitcnt lgkmcnt(8)
	s_barrier
	s_waitcnt lgkmcnt(0)
	s_setprio 1
	s_waitcnt lgkmcnt(0)
	v_mfma_f32_16x16x128_f8f6f4 v[174:177], v[134:141], v[150:157], v[2:5]
	v_mfma_f32_16x16x128_f8f6f4 v[178:181], v[142:149], v[150:157], v[6:9]
	v_mfma_f32_16x16x128_f8f6f4 v[182:185], v[134:141], v[158:165], v[10:13]
	v_mfma_f32_16x16x128_f8f6f4 v[186:189], v[142:149], v[158:165], v[14:17]
	v_mfma_f32_16x16x128_f8f6f4 v[190:193], v[134:141], v[166:173], v[18:21]
	v_mfma_f32_16x16x128_f8f6f4 v[194:197], v[142:149], v[166:173], v[22:25]
	v_mfma_f32_16x16x128_f8f6f4 v[198:201], v[134:141], v[234:241], v[26:29]
	v_mfma_f32_16x16x128_f8f6f4 v[202:205], v[142:149], v[234:241], v[30:33]
	s_setprio 0
	s_barrier
	s_mov_b64 s[4:5], s[42:43]
	v_mov_b32_e32 v2, v230
	s_mov_b32 m0, s16
	ds_read_b128 v[242:245], v232 offset:16384
	ds_read_b128 v[246:249], v232 offset:17408
	ds_read_b128 v[208:211], v232 offset:18432
	ds_read_b128 v[212:215], v232 offset:19456
	s_nop 0
	global_load_lds_dwordx4 v2, s[4:5]
	s_add_u32 s4, s42, 0x20000
	s_addc_u32 s5, s43, 0
	v_mov_b32_e32 v2, v230
	s_mov_b32 m0, s17
	s_nop 0
	global_load_lds_dwordx4 v2, s[4:5]
	s_barrier
	s_waitcnt lgkmcnt(0)
	s_setprio 1
	s_waitcnt lgkmcnt(0)
	v_mfma_f32_16x16x128_f8f6f4 v[2:5], v[242:249], v[150:157], v[34:37]
	v_mfma_f32_16x16x128_f8f6f4 v[6:9], v[208:215], v[150:157], v[38:41]
	v_mfma_f32_16x16x128_f8f6f4 v[10:13], v[242:249], v[158:165], v[42:45]
	v_mfma_f32_16x16x128_f8f6f4 v[14:17], v[208:215], v[158:165], v[46:49]
	v_mfma_f32_16x16x128_f8f6f4 v[18:21], v[242:249], v[166:173], v[50:53]
	v_mfma_f32_16x16x128_f8f6f4 v[22:25], v[208:215], v[166:173], v[54:57]
	v_mfma_f32_16x16x128_f8f6f4 v[26:29], v[242:249], v[234:241], v[58:61]
	v_mfma_f32_16x16x128_f8f6f4 v[30:33], v[208:215], v[234:241], v[62:65]
	s_setprio 0
	s_mov_b64 s[4:5], s[44:45]
	v_mov_b32_e32 v34, v229
	s_mov_b32 m0, s15
	s_barrier
	s_nop 0
	ds_read_b128 v[58:61], v231 offset:16384
	ds_read_b128 v[62:65], v231 offset:17408
	ds_read_b128 v[154:157], v231 offset:18432
	ds_read_b128 v[158:161], v231 offset:19456
	ds_read_b128 v[162:165], v231 offset:20480
	ds_read_b128 v[166:169], v231 offset:21504
	ds_read_b128 v[234:237], v231 offset:22528
	ds_read_b128 v[238:241], v231 offset:23552
	s_nop 0
	global_load_lds_dwordx4 v34, s[4:5]
	s_add_u32 s4, s44, 0x10000
	s_addc_u32 s5, s45, 0
	v_mov_b32_e32 v34, v229
	s_mov_b32 m0, s24
	s_nop 0
	global_load_lds_dwordx4 v34, s[4:5]
	s_barrier
	s_waitcnt lgkmcnt(0)
	s_setprio 1
	s_waitcnt lgkmcnt(0)
	v_mfma_f32_16x16x128_f8f6f4 v[34:37], v[134:141], v[58:65], v[66:69]
	v_mfma_f32_16x16x128_f8f6f4 v[38:41], v[142:149], v[58:65], v[70:73]
	v_mfma_f32_16x16x128_f8f6f4 v[42:45], v[134:141], v[154:161], v[74:77]
	v_mfma_f32_16x16x128_f8f6f4 v[50:53], v[142:149], v[154:161], v[78:81]
	v_mfma_f32_16x16x128_f8f6f4 v[54:57], v[134:141], v[162:169], v[82:85]
	v_mfma_f32_16x16x128_f8f6f4 v[130:133], v[142:149], v[162:169], v[86:89]
	v_mfma_f32_16x16x128_f8f6f4 v[134:137], v[134:141], v[234:241], v[90:93]
	v_mfma_f32_16x16x128_f8f6f4 v[138:141], v[142:149], v[234:241], v[94:97]
	s_setprio 0
	s_barrier
	s_add_u32 s4, s42, 0x8000
	s_addc_u32 s5, s43, 0
	v_mov_b32_e32 v46, v230
	s_mov_b32 m0, s25
	s_nop 0
	global_load_lds_dwordx4 v46, s[4:5]
	s_add_u32 s4, s42, 0x28000
	s_addc_u32 s5, s43, 0
	v_mov_b32_e32 v46, v230
	s_mov_b32 m0, s26
	s_nop 0
	global_load_lds_dwordx4 v46, s[4:5]
	s_waitcnt vmcnt(6)
	s_barrier
	s_setprio 1
	v_mfma_f32_16x16x128_f8f6f4 v[142:145], v[242:249], v[58:65], v[98:101]
	v_mfma_f32_16x16x128_f8f6f4 v[146:149], v[208:215], v[58:65], v[102:105]
	v_mfma_f32_16x16x128_f8f6f4 v[150:153], v[242:249], v[154:161], v[106:109]
	v_mfma_f32_16x16x128_f8f6f4 v[154:157], v[208:215], v[154:161], v[110:113]
	v_mfma_f32_16x16x128_f8f6f4 v[158:161], v[242:249], v[162:169], v[114:117]
	v_mfma_f32_16x16x128_f8f6f4 v[162:165], v[208:215], v[162:169], v[118:121]
	v_mfma_f32_16x16x128_f8f6f4 v[166:169], v[242:249], v[234:241], v[122:125]
	v_mfma_f32_16x16x128_f8f6f4 v[170:173], v[208:215], v[234:241], v[126:129]
	s_setprio 0
	s_barrier
	ds_read_b128 v[208:211], v232 offset:32768
	ds_read_b128 v[212:215], v232 offset:33792
	ds_read_b128 v[234:237], v232 offset:34816
	ds_read_b128 v[238:241], v232 offset:35840
	s_add_u32 s4, s44, 0x20000
	s_addc_u32 s5, s45, 0
	v_mov_b32_e32 v46, v229
	s_mov_b32 m0, s27
	ds_read_b128 v[58:61], v231 offset:32768
	ds_read_b128 v[62:65], v231 offset:33792
	ds_read_b128 v[242:245], v231 offset:34816
	ds_read_b128 v[246:249], v231 offset:35840
	ds_read_b128 v[216:219], v231 offset:36864
	ds_read_b128 v[220:223], v231 offset:37888
	ds_read_b128 v[66:69], v231 offset:38912
	ds_read_b128 v[70:73], v231 offset:39936
	s_nop 0
	global_load_lds_dwordx4 v46, s[4:5]
	s_add_u32 s4, s44, 0x30000
	s_addc_u32 s5, s45, 0
	v_mov_b32_e32 v46, v229
	s_mov_b32 m0, s29
	s_nop 0
	global_load_lds_dwordx4 v46, s[4:5]
	s_waitcnt lgkmcnt(8)
	s_barrier
	s_waitcnt lgkmcnt(0)
	s_setprio 1
	s_waitcnt lgkmcnt(0)
	v_mfma_f32_16x16x128_f8f6f4 v[126:129], v[208:215], v[58:65], v[174:177]
	v_mfma_f32_16x16x128_f8f6f4 v[122:125], v[234:241], v[58:65], v[178:181]
	v_mfma_f32_16x16x128_f8f6f4 v[106:109], v[208:215], v[242:249], v[182:185]
	v_mfma_f32_16x16x128_f8f6f4 v[98:101], v[234:241], v[242:249], v[186:189]
	v_mfma_f32_16x16x128_f8f6f4 v[90:93], v[208:215], v[216:223], v[190:193]
	v_mfma_f32_16x16x128_f8f6f4 v[82:85], v[234:241], v[216:223], v[194:197]
	v_mfma_f32_16x16x128_f8f6f4 v[74:77], v[208:215], v[66:73], v[198:201]
	v_mfma_f32_16x16x128_f8f6f4 v[174:177], v[234:241], v[66:73], v[202:205]
	s_setprio 0
	s_barrier
	s_add_u32 s4, s42, 0x80
	s_addc_u32 s5, s43, 0
	v_mov_b32_e32 v46, v230
	s_mov_b32 m0, s35
	ds_read_b128 v[178:181], v232 offset:49152
	ds_read_b128 v[182:185], v232 offset:50176
	ds_read_b128 v[186:189], v232 offset:51200
	ds_read_b128 v[190:193], v232 offset:52224
	s_nop 0
	global_load_lds_dwordx4 v46, s[4:5]
	s_add_u32 s4, s42, 0x20080
	s_addc_u32 s5, s43, 0
	v_mov_b32_e32 v46, v230
	s_mov_b32 m0, s36
	s_nop 0
	global_load_lds_dwordx4 v46, s[4:5]
	s_barrier
	s_waitcnt lgkmcnt(0)
	s_setprio 1
	s_waitcnt lgkmcnt(0)
	v_mfma_f32_16x16x128_f8f6f4 v[118:121], v[178:185], v[58:65], v[2:5]
	v_mfma_f32_16x16x128_f8f6f4 v[114:117], v[186:193], v[58:65], v[6:9]
	v_mfma_f32_16x16x128_f8f6f4 v[110:113], v[178:185], v[242:249], v[10:13]
	v_mfma_f32_16x16x128_f8f6f4 v[102:105], v[186:193], v[242:249], v[14:17]
	v_mfma_f32_16x16x128_f8f6f4 v[94:97], v[178:185], v[216:223], v[18:21]
	v_mfma_f32_16x16x128_f8f6f4 v[86:89], v[186:193], v[216:223], v[22:25]
	v_mfma_f32_16x16x128_f8f6f4 v[78:81], v[178:185], v[66:73], v[26:29]
	v_mfma_f32_16x16x128_f8f6f4 v[70:73], v[186:193], v[66:73], v[30:33]
	s_setprio 0
	v_mov_b32_e32 v2, v229
	s_mov_b32 m0, s37
	s_barrier
	ds_read_b128 v[6:9], v231 offset:49152
	ds_read_b128 v[10:13], v231 offset:50176
	ds_read_b128 v[18:21], v231 offset:51200
	ds_read_b128 v[22:25], v231 offset:52224
	ds_read_b128 v[194:197], v231 offset:53248
	ds_read_b128 v[198:201], v231 offset:54272
	ds_read_b128 v[216:219], v231 offset:55296
	ds_read_b128 v[220:223], v231 offset:56320
	s_nop 0
	global_load_lds_dwordx4 v2, s[0:1]
	s_add_u32 s0, s44, 0x10080
	s_addc_u32 s1, s45, 0
	v_mov_b32_e32 v2, v229
	s_mov_b32 m0, s70
	s_nop 0
	global_load_lds_dwordx4 v2, s[0:1]
	s_barrier
	s_waitcnt lgkmcnt(0)
	s_setprio 1
	s_waitcnt lgkmcnt(0)
	v_mfma_f32_16x16x128_f8f6f4 v[62:65], v[208:215], v[6:13], v[34:37]
	v_mfma_f32_16x16x128_f8f6f4 v[58:61], v[234:241], v[6:13], v[38:41]
	v_mfma_f32_16x16x128_f8f6f4 v[46:49], v[208:215], v[18:25], v[42:45]
	v_mfma_f32_16x16x128_f8f6f4 v[42:45], v[234:241], v[18:25], v[50:53]
	v_mfma_f32_16x16x128_f8f6f4 v[30:33], v[208:215], v[194:201], v[54:57]
	v_mfma_f32_16x16x128_f8f6f4 v[26:29], v[234:241], v[194:201], v[130:133]
	v_mfma_f32_16x16x128_f8f6f4 v[2:5], v[208:215], v[216:223], v[134:137]
	v_mfma_f32_16x16x128_f8f6f4 v[14:17], v[234:241], v[216:223], v[138:141]
	s_setprio 0
	s_barrier
	s_add_u32 s0, s42, 0x8080
	s_addc_u32 s1, s43, 0
	v_mov_b32_e32 v34, v230
	s_mov_b32 m0, s71
	s_nop 0
	global_load_lds_dwordx4 v34, s[0:1]
	s_add_u32 s0, s42, 0x28080
	s_addc_u32 s1, s43, 0
	v_mov_b32_e32 v34, v230
	s_mov_b32 m0, s72
	s_nop 0
	global_load_lds_dwordx4 v34, s[0:1]
	s_waitcnt vmcnt(6)
	s_barrier
	s_setprio 1
	v_mfma_f32_16x16x128_f8f6f4 v[54:57], v[178:185], v[6:13], v[142:145]
	v_mfma_f32_16x16x128_f8f6f4 v[50:53], v[186:193], v[6:13], v[146:149]
	v_mfma_f32_16x16x128_f8f6f4 v[38:41], v[178:185], v[18:25], v[150:153]
	v_mfma_f32_16x16x128_f8f6f4 v[34:37], v[186:193], v[18:25], v[154:157]
	v_mfma_f32_16x16x128_f8f6f4 v[22:25], v[178:185], v[194:201], v[158:161]
	v_mfma_f32_16x16x128_f8f6f4 v[18:21], v[186:193], v[194:201], v[162:165]
	v_mfma_f32_16x16x128_f8f6f4 v[10:13], v[178:185], v[216:223], v[166:169]
	v_mfma_f32_16x16x128_f8f6f4 v[6:9], v[186:193], v[216:223], v[170:173]
	s_setprio 0
	s_andn2_b64 vcc, exec, s[54:55]
	s_barrier
	s_cbranch_vccnz .LBB0_123
	s_barrier
.LBB0_123:
	s_lshl_b32 s0, s73, 2
	s_or_b32 s0, s0, s8
	s_mul_hi_i32 s1, s0, 0x2aaaaaab
	s_lshr_b32 s4, s1, 31
	s_ashr_i32 s1, s1, 2
	s_add_i32 s1, s1, s4
	s_mul_i32 s4, s1, 24
	s_sub_i32 s4, s0, s4
	s_ashr_i32 s4, s4, 3
	s_lshl_b32 s6, s4, 6
	s_add_i32 s5, s0, 23
	s_ashr_i32 s7, s6, 31
	s_cmp_lt_u32 s5, 47
	v_mov_b32_e32 v135, v0
	s_cselect_b64 s[46:47], -1, 0
	v_mov_b32_e32 v66, 0x3e38aa3b
	v_cndmask_b32_e64 v130, 1.0, v66, s[46:47]
	v_lshrrev_b32_e32 v66, 1, v135
	v_and_b32_e32 v138, 24, v66
	v_mul_f32_e32 v66, v127, v127
	v_mul_f32_e32 v67, v129, v129
	v_fmac_f32_e32 v66, v126, v126
	v_fmac_f32_e32 v67, v128, v128
	v_add_f32_e32 v66, v66, v67
	v_mul_f32_e32 v67, v123, v123
	v_mul_f32_e32 v68, v125, v125
	v_fmac_f32_e32 v67, v122, v122
	v_fmac_f32_e32 v68, v124, v124
	v_add_f32_e32 v67, v67, v68
	v_add_f32_e32 v66, v66, v67
	v_mul_f32_e32 v67, v119, v119
	v_mul_f32_e32 v68, v121, v121
	v_fmac_f32_e32 v67, v118, v118
	v_fmac_f32_e32 v68, v120, v120
	v_add_f32_e32 v67, v67, v68
	v_add_f32_e32 v66, v66, v67
	v_mul_f32_e32 v67, v115, v115
	v_mul_f32_e32 v68, v117, v117
	s_and_b64 s[42:43], s[46:47], exec
	v_fmac_f32_e32 v67, v114, v114
	v_fmac_f32_e32 v68, v116, v116
	s_cselect_b32 s23, s48, s50
	v_add_f32_e32 v67, v67, v68
	s_cselect_b32 s5, s49, s51
	s_add_u32 s23, s23, s56
	v_add_f32_e32 v66, v66, v67
	s_addc_u32 s5, s5, s57
	s_lshl_b64 s[6:7], s[6:7], 2
	v_mov_b32_e32 v67, v66
	s_add_u32 s6, s23, s6
	s_nop 0
	v_permlane16_swap_b32_e32 v66, v67
	s_addc_u32 s7, s5, s7
	v_add_f32_e32 v134, v66, v67
	s_cmp_lt_i32 s0, 48
	v_lshlrev_b32_e32 v206, 2, v138
	v_mov_b32_e32 v139, v134
	v_mov_b32_e32 v136, 1.0
	s_cselect_b64 s[44:45], -1, 0
	s_cmp_gt_i32 s0, 47
	v_lshl_add_u64 v[132:133], s[6:7], 0, v[206:207]
	v_mov_b32_e32 v131, v130
	v_permlane32_swap_b32_e32 v134, v139
	v_mov_b32_e32 v148, 1.0
	v_mov_b32_e32 v149, 1.0
	v_mov_b32_e32 v152, 1.0
	v_mov_b32_e32 v153, 1.0
	v_mov_b32_e32 v146, 1.0
	v_mov_b32_e32 v147, 1.0
	v_mov_b32_e32 v150, 1.0
	v_mov_b32_e32 v151, 1.0
	s_cbranch_scc1 .LBB0_125
	global_load_dwordx4 v[156:159], v[132:133], off
	global_load_dwordx4 v[160:163], v[132:133], off offset:16
	global_load_dwordx4 v[164:167], v[132:133], off offset:128
	global_load_dwordx4 v[168:171], v[132:133], off offset:144
	v_mov_b32_e32 v144, v130
	v_mov_b32_e32 v145, v130
	s_waitcnt vmcnt(0)
	v_mov_b64_e32 v[66:67], v[156:157]
	v_mov_b64_e32 v[68:69], v[158:159]
	v_mov_b64_e32 v[140:141], v[160:161]
	v_mov_b64_e32 v[142:143], v[162:163]
	v_pk_mul_f32 v[152:153], v[144:145], v[68:69]
	v_pk_mul_f32 v[148:149], v[130:131], v[66:67]
	v_pk_mul_f32 v[150:151], v[144:145], v[142:143]
	v_pk_mul_f32 v[146:147], v[130:131], v[140:141]
.LBB0_125:
	v_cndmask_b32_e64 v66, 0, 1, s[44:45]
	v_cmp_ne_u32_e64 s[42:43], 1, v66
	s_andn2_b64 vcc, exec, s[44:45]
	v_mov_b32_e32 v137, 1.0
	v_mov_b32_e32 v144, 1.0
	v_mov_b32_e32 v145, 1.0
	v_mov_b32_e32 v140, 1.0
	v_mov_b32_e32 v141, 1.0
	v_mov_b32_e32 v142, 1.0
	v_mov_b32_e32 v143, 1.0
	s_cbranch_vccnz .LBB0_127
	v_mov_b64_e32 v[66:67], v[164:165]
	v_mov_b64_e32 v[68:69], v[166:167]
	v_mov_b64_e32 v[140:141], v[168:169]
	v_mov_b64_e32 v[142:143], v[170:171]
	v_mov_b32_e32 v154, v130
	v_mov_b32_e32 v155, v130
	v_pk_mul_f32 v[144:145], v[154:155], v[68:69]
	v_pk_mul_f32 v[136:137], v[130:131], v[66:67]
	v_pk_mul_f32 v[142:143], v[154:155], v[142:143]
	v_pk_mul_f32 v[140:141], v[130:131], v[140:141]
.LBB0_127:
	v_add_f32_e32 v66, v134, v139
	v_fmamk_f32 v66, v66, 0x37800000, v225
	v_mul_f32_e32 v66, 0x3c800000, v66
	v_rsq_f32_e32 v66, v66
	v_mov_b32_e32 v67, 0x3d800000
	v_cndmask_b32_e64 v154, v67, v228, s[46:47]
	s_mul_i32 s1, s1, 3
	v_cndmask_b32_e64 v66, 1.0, v66, s[44:45]
	v_mul_f32_e32 v66, v154, v66
	v_pk_mul_f32 v[68:69], v[126:127], v[66:67] op_sel_hi:[1,0]
	v_pk_mul_f32 v[126:127], v[128:129], v[66:67] op_sel_hi:[1,0]
	v_pk_mul_f32 v[68:69], v[68:69], v[148:149]
	v_pk_mul_f32 v[122:123], v[122:123], v[66:67] op_sel_hi:[1,0]
	v_pk_mul_f32 v[124:125], v[124:125], v[66:67] op_sel_hi:[1,0]
	v_min_f32_e64 v67, |v68|, s33
	v_bfi_b32 v67, s2, v67, v68
	v_min_f32_e64 v68, |v69|, s33
	v_bfi_b32 v68, s2, v68, v69
	v_mov_b32_e32 v128, v207
	v_cvt_pk_fp8_f32 v128, v67, v68
	v_pk_mul_f32 v[126:127], v[126:127], v[152:153]
	v_pk_mul_f32 v[122:123], v[122:123], v[146:147]
	v_min_f32_e64 v69, |v126|, s33
	v_min_f32_e64 v68, |v127|, s33
	v_bfi_b32 v67, s2, v69, v126
	v_bfi_b32 v68, s2, v68, v127
	v_cvt_pk_fp8_f32 v128, v67, v68 op_sel:[0,0,1]
	v_min_f32_e64 v67, |v122|, s33
	v_min_f32_e64 v68, |v123|, s33
	v_bfi_b32 v67, s2, v67, v122
	v_bfi_b32 v68, s2, v68, v123
	v_mov_b32_e32 v126, v207
	v_cvt_pk_fp8_f32 v126, v67, v68
	v_pk_mul_f32 v[124:125], v[124:125], v[150:151]
	s_add_i32 s4, s1, s4
	v_min_f32_e64 v69, |v124|, s33
	v_min_f32_e64 v68, |v125|, s33
	v_bfi_b32 v67, s2, v69, v124
	v_bfi_b32 v68, s2, v68, v125
	v_cvt_pk_fp8_f32 v126, v67, v68 op_sel:[0,0,1]
	v_lshlrev_b32_e32 v67, 2, v135
	v_pk_mul_f32 v[118:119], v[118:119], v[66:67] op_sel_hi:[1,0]
	v_and_b32_e32 v206, 32, v67
	v_pk_mul_f32 v[118:119], v[118:119], v[136:137]
	v_pk_mul_f32 v[120:121], v[120:121], v[66:67] op_sel_hi:[1,0]
	v_pk_mul_f32 v[114:115], v[114:115], v[66:67] op_sel_hi:[1,0]
	v_pk_mul_f32 v[66:67], v[116:117], v[66:67] op_sel_hi:[1,0]
	v_min_f32_e64 v116, |v118|, s33
	v_bfi_b32 v117, s2, v116, v118
	v_min_f32_e64 v116, |v119|, s33
	v_bfi_b32 v118, s2, v116, v119
	v_mov_b32_e32 v116, v207
	v_cvt_pk_fp8_f32 v116, v117, v118
	v_pk_mul_f32 v[120:121], v[120:121], v[144:145]
	s_ashr_i32 s5, s4, 31
	v_min_f32_e64 v119, |v120|, s33
	v_min_f32_e64 v118, |v121|, s33
	s_lshl_b64 s[4:5], s[4:5], 24
	v_pk_mul_f32 v[114:115], v[114:115], v[140:141]
	v_bfi_b32 v117, s2, v119, v120
	v_bfi_b32 v118, s2, v118, v121
	s_add_u32 s1, s31, s4
	v_cvt_pk_fp8_f32 v116, v117, v118 op_sel:[0,0,1]
	v_min_f32_e64 v117, |v114|, s33
	s_addc_u32 s4, s34, s5
	s_lshl_b32 s0, s0, 18
	v_bfi_b32 v114, s2, v117, v114
	v_min_f32_e64 v117, |v115|, s33
	s_and_b32 s0, s0, 0x1c0000
	v_bfi_b32 v115, s2, v117, v115
	v_mov_b32_e32 v117, v207
	s_add_u32 s0, s1, s0
	v_cvt_pk_fp8_f32 v117, v114, v115
	s_addc_u32 s1, s4, 0
	v_pk_mul_f32 v[66:67], v[66:67], v[142:143]
	v_lshl_add_u64 v[68:69], s[0:1], 0, v[206:207]
	s_lshl_b32 s0, s10, 8
	v_min_f32_e64 v118, |v66|, s33
	v_min_f32_e64 v114, |v67|, s33
	s_add_i32 s0, s0, s30
	v_bfi_b32 v66, s2, v118, v66
	v_bfi_b32 v67, s2, v114, v67
	v_and_b32_e32 v146, 15, v135
	s_ashr_i32 s4, s0, 12
	v_cvt_pk_fp8_f32 v117, v66, v67 op_sel:[0,0,1]
	v_mov_b32_e32 v139, v207
	v_or_b32_e32 v124, s0, v146
	s_ashr_i32 s5, s4, 31
	v_lshl_add_u64 v[122:123], v[68:69], 0, v[138:139]
	s_lshl_b64 s[4:5], s[4:5], 21
	v_lshlrev_b32_e32 v114, 6, v124
	v_lshl_add_u64 v[68:69], v[122:123], 0, s[4:5]
	v_mov_b32_e32 v66, v128
	v_mov_b32_e32 v67, v126
	v_and_b32_e32 v206, 0x3f1c0, v114
	v_mov_b32_dpp v66, v116 row_ror:8 row_mask:0xf bank_mask:0xc
	v_mov_b32_dpp v67, v117 row_ror:8 row_mask:0xf bank_mask:0xc
	v_lshl_add_u64 v[114:115], v[68:69], 0, v[206:207]
	v_mov_b32_dpp v116, v128 row_ror:8 row_mask:0xf bank_mask:0x3
	v_mov_b32_dpp v117, v126 row_ror:8 row_mask:0xf bank_mask:0x3
	global_store_dwordx2 v[114:115], v[66:67], off
	global_store_dwordx2 v[114:115], v[116:117], off offset:512
	v_mul_f32_e32 v66, v107, v107
	v_mul_f32_e32 v67, v109, v109
	v_fmac_f32_e32 v66, v106, v106
	v_fmac_f32_e32 v67, v108, v108
	v_add_f32_e32 v66, v66, v67
	v_mul_f32_e32 v67, v99, v99
	v_mul_f32_e32 v68, v101, v101
	v_fmac_f32_e32 v67, v98, v98
	v_fmac_f32_e32 v68, v100, v100
	v_add_f32_e32 v67, v67, v68
	v_add_f32_e32 v66, v66, v67
	v_mul_f32_e32 v67, v111, v111
	v_mul_f32_e32 v68, v113, v113
	v_fmac_f32_e32 v67, v110, v110
	v_fmac_f32_e32 v68, v112, v112
	v_add_f32_e32 v67, v67, v68
	v_add_f32_e32 v66, v66, v67
	v_mul_f32_e32 v67, v103, v103
	v_mul_f32_e32 v68, v105, v105
	v_fmac_f32_e32 v67, v102, v102
	v_fmac_f32_e32 v68, v104, v104
	v_add_f32_e32 v67, v67, v68
	v_add_f32_e32 v66, v66, v67
	v_mov_b32_e32 v67, v66
	s_nop 1
	v_permlane16_swap_b32_e32 v66, v67
	v_add_f32_e32 v116, v66, v67
	v_mov_b32_e32 v117, v116
	v_mov_b32_e32 v134, 1.0
	s_nop 0
	v_permlane32_swap_b32_e32 v116, v117
	s_and_b64 vcc, exec, s[42:43]
	v_mov_b32_e32 v124, 1.0
	v_mov_b32_e32 v125, 1.0
	v_mov_b32_e32 v138, 1.0
	v_mov_b32_e32 v139, 1.0
	v_mov_b32_e32 v120, 1.0
	v_mov_b32_e32 v121, 1.0
	v_mov_b32_e32 v128, 1.0
	v_mov_b32_e32 v129, 1.0
	s_cbranch_vccnz .LBB0_129
	v_mov_b64_e32 v[66:67], v[156:157]
	v_mov_b64_e32 v[68:69], v[158:159]
	v_mov_b64_e32 v[118:119], v[160:161]
	v_mov_b64_e32 v[120:121], v[162:163]
	v_mov_b32_e32 v126, v130
	v_mov_b32_e32 v127, v130
	v_pk_mul_f32 v[138:139], v[126:127], v[68:69]
	v_pk_mul_f32 v[124:125], v[130:131], v[66:67]
	v_pk_mul_f32 v[128:129], v[126:127], v[120:121]
	v_pk_mul_f32 v[120:121], v[130:131], v[118:119]
.LBB0_129:
	s_and_b64 vcc, exec, s[42:43]
	v_mov_b32_e32 v135, 1.0
	v_mov_b32_e32 v136, 1.0
	v_mov_b32_e32 v137, 1.0
	v_mov_b32_e32 v118, 1.0
	v_mov_b32_e32 v119, 1.0
	v_mov_b32_e32 v126, 1.0
	v_mov_b32_e32 v127, 1.0
	s_cbranch_vccnz .LBB0_131
	v_mov_b64_e32 v[66:67], v[164:165]
	v_mov_b64_e32 v[68:69], v[166:167]
	v_mov_b64_e32 v[140:141], v[168:169]
	v_mov_b64_e32 v[142:143], v[170:171]
	v_mov_b32_e32 v118, v130
	v_mov_b32_e32 v119, v130
	v_pk_mul_f32 v[136:137], v[118:119], v[68:69]
	v_pk_mul_f32 v[134:135], v[130:131], v[66:67]
	v_pk_mul_f32 v[126:127], v[118:119], v[142:143]
	v_pk_mul_f32 v[118:119], v[130:131], v[140:141]
.LBB0_131:
	v_add_f32_e32 v66, v116, v117
	v_fmamk_f32 v66, v66, 0x37800000, v225
	v_mul_f32_e32 v66, 0x3c800000, v66
	v_rsq_f32_e32 v66, v66
	v_mov_b32_e32 v116, 1.0
	s_and_b64 vcc, exec, s[42:43]
	v_cndmask_b32_e64 v66, 1.0, v66, s[44:45]
	v_mul_f32_e32 v66, v154, v66
	v_pk_mul_f32 v[106:107], v[106:107], v[66:67] op_sel_hi:[1,0]
	v_pk_mul_f32 v[68:69], v[108:109], v[66:67] op_sel_hi:[1,0]
	v_pk_mul_f32 v[106:107], v[106:107], v[124:125]
	v_pk_mul_f32 v[100:101], v[100:101], v[66:67] op_sel_hi:[1,0]
	v_pk_mul_f32 v[98:99], v[98:99], v[66:67] op_sel_hi:[1,0]
	v_min_f32_e64 v67, |v106|, s33
	v_bfi_b32 v67, s2, v67, v106
	v_min_f32_e64 v106, |v107|, s33
	v_bfi_b32 v106, s2, v106, v107
	v_mov_b32_e32 v108, v207
	v_pk_mul_f32 v[68:69], v[68:69], v[138:139]
	v_cvt_pk_fp8_f32 v108, v67, v106
	v_min_f32_e64 v107, |v68|, s33
	v_bfi_b32 v67, s2, v107, v68
	v_min_f32_e64 v68, |v69|, s33
	v_pk_mul_f32 v[98:99], v[98:99], v[120:121]
	v_bfi_b32 v68, s2, v68, v69
	v_cvt_pk_fp8_f32 v108, v67, v68 op_sel:[0,0,1]
	v_min_f32_e64 v67, |v98|, s33
	v_min_f32_e64 v68, |v99|, s33
	v_pk_mul_f32 v[100:101], v[100:101], v[128:129]
	v_bfi_b32 v67, s2, v67, v98
	v_bfi_b32 v68, s2, v68, v99
	v_mov_b32_e32 v106, v207
	v_min_f32_e64 v69, |v100|, s33
	v_cvt_pk_fp8_f32 v106, v67, v68
	v_bfi_b32 v67, s2, v69, v100
	v_min_f32_e64 v68, |v101|, s33
	v_pk_mul_f32 v[98:99], v[110:111], v[66:67] op_sel_hi:[1,0]
	v_bfi_b32 v68, s2, v68, v101
	v_pk_mul_f32 v[98:99], v[98:99], v[134:135]
	v_cvt_pk_fp8_f32 v106, v67, v68 op_sel:[0,0,1]
	v_pk_mul_f32 v[68:69], v[112:113], v[66:67] op_sel_hi:[1,0]
	v_pk_mul_f32 v[100:101], v[104:105], v[66:67] op_sel_hi:[1,0]
	v_pk_mul_f32 v[66:67], v[102:103], v[66:67] op_sel_hi:[1,0]
	v_min_f32_e64 v102, |v98|, s33
	v_bfi_b32 v102, s2, v102, v98
	v_min_f32_e64 v98, |v99|, s33
	v_bfi_b32 v99, s2, v98, v99
	v_mov_b32_e32 v98, v207
	v_cvt_pk_fp8_f32 v98, v102, v99
	v_pk_mul_f32 v[68:69], v[68:69], v[136:137]
	v_pk_mul_f32 v[66:67], v[66:67], v[118:119]
	v_min_f32_e64 v103, |v68|, s33
	v_min_f32_e64 v99, |v69|, s33
	v_bfi_b32 v68, s2, v103, v68
	v_bfi_b32 v69, s2, v99, v69
	v_cvt_pk_fp8_f32 v98, v68, v69 op_sel:[0,0,1]
	v_min_f32_e64 v68, |v66|, s33
	v_bfi_b32 v66, s2, v68, v66
	v_min_f32_e64 v68, |v67|, s33
	v_bfi_b32 v67, s2, v68, v67
	v_mov_b32_e32 v99, v207
	v_cvt_pk_fp8_f32 v99, v66, v67
	v_pk_mul_f32 v[100:101], v[100:101], v[126:127]
	v_mov_b32_e32 v104, 1.0
	v_min_f32_e64 v68, |v100|, s33
	v_min_f32_e64 v67, |v101|, s33
	v_bfi_b32 v66, s2, v68, v100
	v_bfi_b32 v67, s2, v67, v101
	v_cvt_pk_fp8_f32 v99, v66, v67 op_sel:[0,0,1]
	v_mov_b32_e32 v66, v108
	v_mov_b32_e32 v67, v106
	v_mul_f32_e32 v68, v85, v85
	v_mov_b32_dpp v66, v98 row_ror:8 row_mask:0xf bank_mask:0xc
	v_mov_b32_dpp v67, v99 row_ror:8 row_mask:0xf bank_mask:0xc
	v_mov_b32_dpp v98, v108 row_ror:8 row_mask:0xf bank_mask:0x3
	v_mov_b32_dpp v99, v106 row_ror:8 row_mask:0xf bank_mask:0x3
	global_store_dwordx2 v[114:115], v[66:67], off offset:1024
	global_store_dwordx2 v[114:115], v[98:99], off offset:1536
	v_mul_f32_e32 v66, v91, v91
	v_mul_f32_e32 v67, v93, v93
	v_fmac_f32_e32 v66, v90, v90
	v_fmac_f32_e32 v67, v92, v92
	v_add_f32_e32 v66, v66, v67
	v_mul_f32_e32 v67, v83, v83
	v_fmac_f32_e32 v67, v82, v82
	v_fmac_f32_e32 v68, v84, v84
	v_add_f32_e32 v67, v67, v68
	v_add_f32_e32 v66, v66, v67
	v_mul_f32_e32 v67, v95, v95
	v_mul_f32_e32 v68, v97, v97
	v_fmac_f32_e32 v67, v94, v94
	v_fmac_f32_e32 v68, v96, v96
	v_add_f32_e32 v67, v67, v68
	v_add_f32_e32 v66, v66, v67
	v_mul_f32_e32 v67, v87, v87
	v_mul_f32_e32 v68, v89, v89
	v_fmac_f32_e32 v67, v86, v86
	v_fmac_f32_e32 v68, v88, v88
	v_add_f32_e32 v67, v67, v68
	v_add_f32_e32 v66, v66, v67
	v_mov_b32_e32 v67, v66
	s_nop 1
	v_permlane16_swap_b32_e32 v66, v67
	v_add_f32_e32 v98, v66, v67
	v_mov_b32_e32 v99, v98
	s_nop 1
	v_permlane32_swap_b32_e32 v98, v99
	v_mov_b32_e32 v105, 1.0
	v_mov_b32_e32 v112, 1.0
	v_mov_b32_e32 v113, 1.0
	v_mov_b32_e32 v102, 1.0
	v_mov_b32_e32 v103, 1.0
	v_mov_b32_e32 v108, 1.0
	v_mov_b32_e32 v109, 1.0
	s_cbranch_vccnz .LBB0_133
	v_mov_b64_e32 v[66:67], v[156:157]
	v_mov_b64_e32 v[68:69], v[158:159]
	v_mov_b64_e32 v[100:101], v[160:161]
	v_mov_b64_e32 v[102:103], v[162:163]
	v_mov_b32_e32 v106, v130
	v_mov_b32_e32 v107, v130
	v_pk_mul_f32 v[112:113], v[106:107], v[68:69]
	v_pk_mul_f32 v[104:105], v[130:131], v[66:67]
	v_pk_mul_f32 v[108:109], v[106:107], v[102:103]
	v_pk_mul_f32 v[102:103], v[130:131], v[100:101]
.LBB0_133:
	s_and_b64 vcc, exec, s[42:43]
	v_mov_b32_e32 v117, 1.0
	v_mov_b32_e32 v110, 1.0
	v_mov_b32_e32 v111, 1.0
	v_mov_b32_e32 v100, 1.0
	v_mov_b32_e32 v101, 1.0
	v_mov_b32_e32 v106, 1.0
	v_mov_b32_e32 v107, 1.0
	s_cbranch_vccnz .LBB0_135
	v_mov_b64_e32 v[66:67], v[164:165]
	v_mov_b64_e32 v[68:69], v[166:167]
	v_mov_b64_e32 v[118:119], v[168:169]
	v_mov_b64_e32 v[120:121], v[170:171]
	v_mov_b32_e32 v100, v130
	v_mov_b32_e32 v101, v130
	v_pk_mul_f32 v[110:111], v[100:101], v[68:69]
	v_pk_mul_f32 v[116:117], v[130:131], v[66:67]
	v_pk_mul_f32 v[106:107], v[100:101], v[120:121]
	v_pk_mul_f32 v[100:101], v[130:131], v[118:119]
.LBB0_135:
	v_add_f32_e32 v66, v98, v99
	v_fmamk_f32 v66, v66, 0x37800000, v225
	v_mul_f32_e32 v66, 0x3c800000, v66
	v_rsq_f32_e32 v66, v66
	v_mov_b32_e32 v98, 1.0
	s_and_b64 vcc, exec, s[42:43]
	v_cndmask_b32_e64 v66, 1.0, v66, s[44:45]
	v_mul_f32_e32 v66, v154, v66
	v_pk_mul_f32 v[90:91], v[90:91], v[66:67] op_sel_hi:[1,0]
	v_pk_mul_f32 v[68:69], v[92:93], v[66:67] op_sel_hi:[1,0]
	v_pk_mul_f32 v[90:91], v[90:91], v[104:105]
	v_pk_mul_f32 v[84:85], v[84:85], v[66:67] op_sel_hi:[1,0]
	v_pk_mul_f32 v[82:83], v[82:83], v[66:67] op_sel_hi:[1,0]
	v_min_f32_e64 v67, |v90|, s33
	v_bfi_b32 v67, s2, v67, v90
	v_min_f32_e64 v90, |v91|, s33
	v_bfi_b32 v90, s2, v90, v91
	v_mov_b32_e32 v92, v207
	v_pk_mul_f32 v[68:69], v[68:69], v[112:113]
	v_cvt_pk_fp8_f32 v92, v67, v90
	v_min_f32_e64 v91, |v68|, s33
	v_bfi_b32 v67, s2, v91, v68
	v_min_f32_e64 v68, |v69|, s33
	v_pk_mul_f32 v[82:83], v[82:83], v[102:103]
	v_bfi_b32 v68, s2, v68, v69
	v_cvt_pk_fp8_f32 v92, v67, v68 op_sel:[0,0,1]
	v_min_f32_e64 v67, |v82|, s33
	v_min_f32_e64 v68, |v83|, s33
	v_pk_mul_f32 v[84:85], v[84:85], v[108:109]
	v_bfi_b32 v67, s2, v67, v82
	v_bfi_b32 v68, s2, v68, v83
	v_mov_b32_e32 v90, v207
	v_min_f32_e64 v69, |v84|, s33
	v_cvt_pk_fp8_f32 v90, v67, v68
	v_bfi_b32 v67, s2, v69, v84
	v_min_f32_e64 v68, |v85|, s33
	v_pk_mul_f32 v[82:83], v[94:95], v[66:67] op_sel_hi:[1,0]
	v_bfi_b32 v68, s2, v68, v85
	v_pk_mul_f32 v[82:83], v[82:83], v[116:117]
	v_cvt_pk_fp8_f32 v90, v67, v68 op_sel:[0,0,1]
	v_pk_mul_f32 v[68:69], v[96:97], v[66:67] op_sel_hi:[1,0]
	v_pk_mul_f32 v[84:85], v[88:89], v[66:67] op_sel_hi:[1,0]
	v_pk_mul_f32 v[66:67], v[86:87], v[66:67] op_sel_hi:[1,0]
	v_min_f32_e64 v86, |v82|, s33
	v_bfi_b32 v86, s2, v86, v82
	v_min_f32_e64 v82, |v83|, s33
	v_bfi_b32 v83, s2, v82, v83
	v_mov_b32_e32 v82, v207
	v_cvt_pk_fp8_f32 v82, v86, v83
	v_pk_mul_f32 v[68:69], v[68:69], v[110:111]
	v_pk_mul_f32 v[66:67], v[66:67], v[100:101]
	v_min_f32_e64 v87, |v68|, s33
	v_min_f32_e64 v83, |v69|, s33
	v_bfi_b32 v68, s2, v87, v68
	v_bfi_b32 v69, s2, v83, v69
	v_cvt_pk_fp8_f32 v82, v68, v69 op_sel:[0,0,1]
	v_min_f32_e64 v68, |v66|, s33
	v_bfi_b32 v66, s2, v68, v66
	v_min_f32_e64 v68, |v67|, s33
	v_bfi_b32 v67, s2, v68, v67
	v_mov_b32_e32 v83, v207
	v_cvt_pk_fp8_f32 v83, v66, v67
	v_pk_mul_f32 v[84:85], v[84:85], v[106:107]
	v_mov_b32_e32 v88, 1.0
	v_min_f32_e64 v68, |v84|, s33
	v_min_f32_e64 v67, |v85|, s33
	v_bfi_b32 v66, s2, v68, v84
	v_bfi_b32 v67, s2, v67, v85
	v_cvt_pk_fp8_f32 v83, v66, v67 op_sel:[0,0,1]
	v_mov_b32_e32 v66, v92
	v_mov_b32_e32 v67, v90
	v_mul_f32_e32 v68, v177, v177
	v_mov_b32_dpp v66, v82 row_ror:8 row_mask:0xf bank_mask:0xc
	v_mov_b32_dpp v67, v83 row_ror:8 row_mask:0xf bank_mask:0xc
	v_mov_b32_dpp v82, v92 row_ror:8 row_mask:0xf bank_mask:0x3
	v_mov_b32_dpp v83, v90 row_ror:8 row_mask:0xf bank_mask:0x3
	global_store_dwordx2 v[114:115], v[66:67], off offset:2048
	global_store_dwordx2 v[114:115], v[82:83], off offset:2560
	v_mul_f32_e32 v66, v75, v75
	v_mul_f32_e32 v67, v77, v77
	v_fmac_f32_e32 v66, v74, v74
	v_fmac_f32_e32 v67, v76, v76
	v_add_f32_e32 v66, v66, v67
	v_mul_f32_e32 v67, v175, v175
	v_fmac_f32_e32 v67, v174, v174
	v_fmac_f32_e32 v68, v176, v176
	v_add_f32_e32 v67, v67, v68
	v_add_f32_e32 v66, v66, v67
	v_mul_f32_e32 v67, v79, v79
	v_mul_f32_e32 v68, v81, v81
	v_fmac_f32_e32 v67, v78, v78
	v_fmac_f32_e32 v68, v80, v80
	v_add_f32_e32 v67, v67, v68
	v_add_f32_e32 v66, v66, v67
	v_mul_f32_e32 v67, v71, v71
	v_mul_f32_e32 v68, v73, v73
	v_fmac_f32_e32 v67, v70, v70
	v_fmac_f32_e32 v68, v72, v72
	v_add_f32_e32 v67, v67, v68
	v_add_f32_e32 v66, v66, v67
	v_mov_b32_e32 v67, v66
	s_nop 1
	v_permlane16_swap_b32_e32 v66, v67
	v_add_f32_e32 v82, v66, v67
	v_mov_b32_e32 v83, v82
	s_nop 1
	v_permlane32_swap_b32_e32 v82, v83
	v_mov_b32_e32 v89, 1.0
	v_mov_b32_e32 v96, 1.0
	v_mov_b32_e32 v97, 1.0
	v_mov_b32_e32 v86, 1.0
	v_mov_b32_e32 v87, 1.0
	v_mov_b32_e32 v92, 1.0
	v_mov_b32_e32 v93, 1.0
	s_cbranch_vccnz .LBB0_137
	v_mov_b64_e32 v[66:67], v[156:157]
	v_mov_b64_e32 v[68:69], v[158:159]
	v_mov_b64_e32 v[84:85], v[160:161]
	v_mov_b64_e32 v[86:87], v[162:163]
	v_mov_b32_e32 v90, v130
	v_mov_b32_e32 v91, v130
	v_pk_mul_f32 v[96:97], v[90:91], v[68:69]
	v_pk_mul_f32 v[88:89], v[130:131], v[66:67]
	v_pk_mul_f32 v[92:93], v[90:91], v[86:87]
	v_pk_mul_f32 v[86:87], v[130:131], v[84:85]
.LBB0_137:
	s_and_b64 vcc, exec, s[42:43]
	v_mov_b32_e32 v99, 1.0
	v_mov_b32_e32 v94, 1.0
	v_mov_b32_e32 v95, 1.0
	v_mov_b32_e32 v84, 1.0
	v_mov_b32_e32 v85, 1.0
	v_mov_b32_e32 v90, 1.0
	v_mov_b32_e32 v91, 1.0
	s_cbranch_vccnz .LBB0_139
	v_mov_b64_e32 v[66:67], v[164:165]
	v_mov_b64_e32 v[68:69], v[166:167]
	v_mov_b64_e32 v[100:101], v[168:169]
	v_mov_b64_e32 v[102:103], v[170:171]
	v_mov_b32_e32 v84, v130
	v_mov_b32_e32 v85, v130
	v_pk_mul_f32 v[94:95], v[84:85], v[68:69]
	v_pk_mul_f32 v[98:99], v[130:131], v[66:67]
	v_pk_mul_f32 v[90:91], v[84:85], v[102:103]
	v_pk_mul_f32 v[84:85], v[130:131], v[100:101]
.LBB0_139:
	v_add_f32_e32 v66, v82, v83
	v_fmamk_f32 v66, v66, 0x37800000, v225
	v_mul_f32_e32 v66, 0x3c800000, v66
	v_rsq_f32_e32 v66, v66
	v_mov_b32_e32 v83, v207
	v_mov_b32_e32 v82, 1.0
	s_and_b64 vcc, exec, s[42:43]
	v_cndmask_b32_e64 v66, 1.0, v66, s[44:45]
	v_mul_f32_e32 v66, v154, v66
	v_pk_mul_f32 v[74:75], v[74:75], v[66:67] op_sel_hi:[1,0]
	v_pk_mul_f32 v[68:69], v[76:77], v[66:67] op_sel_hi:[1,0]
	v_pk_mul_f32 v[74:75], v[74:75], v[88:89]
	v_pk_mul_f32 v[76:77], v[176:177], v[66:67] op_sel_hi:[1,0]
	v_pk_mul_f32 v[88:89], v[174:175], v[66:67] op_sel_hi:[1,0]
	v_min_f32_e64 v67, |v74|, s33
	v_bfi_b32 v67, s2, v67, v74
	v_min_f32_e64 v74, |v75|, s33
	v_bfi_b32 v74, s2, v74, v75
	v_pk_mul_f32 v[68:69], v[68:69], v[96:97]
	v_cvt_pk_fp8_f32 v83, v67, v74
	v_min_f32_e64 v75, |v68|, s33
	v_bfi_b32 v67, s2, v75, v68
	v_min_f32_e64 v68, |v69|, s33
	v_pk_mul_f32 v[86:87], v[88:89], v[86:87]
	v_bfi_b32 v68, s2, v68, v69
	v_cvt_pk_fp8_f32 v83, v67, v68 op_sel:[0,0,1]
	v_min_f32_e64 v67, |v86|, s33
	v_min_f32_e64 v68, |v87|, s33
	v_pk_mul_f32 v[76:77], v[76:77], v[92:93]
	v_bfi_b32 v67, s2, v67, v86
	v_bfi_b32 v68, s2, v68, v87
	v_mov_b32_e32 v86, v207
	v_min_f32_e64 v69, |v76|, s33
	v_cvt_pk_fp8_f32 v86, v67, v68
	v_bfi_b32 v67, s2, v69, v76
	v_min_f32_e64 v68, |v77|, s33
	v_pk_mul_f32 v[74:75], v[78:79], v[66:67] op_sel_hi:[1,0]
	v_bfi_b32 v68, s2, v68, v77
	v_pk_mul_f32 v[74:75], v[74:75], v[98:99]
	v_pk_mul_f32 v[72:73], v[72:73], v[66:67] op_sel_hi:[1,0]
	v_cvt_pk_fp8_f32 v86, v67, v68 op_sel:[0,0,1]
	v_pk_mul_f32 v[68:69], v[80:81], v[66:67] op_sel_hi:[1,0]
	v_pk_mul_f32 v[66:67], v[70:71], v[66:67] op_sel_hi:[1,0]
	v_pk_mul_f32 v[70:71], v[72:73], v[90:91]
	v_min_f32_e64 v72, |v74|, s33
	v_bfi_b32 v73, s2, v72, v74
	v_min_f32_e64 v72, |v75|, s33
	v_bfi_b32 v74, s2, v72, v75
	v_mov_b32_e32 v72, v207
	v_cvt_pk_fp8_f32 v72, v73, v74
	v_pk_mul_f32 v[68:69], v[68:69], v[94:95]
	v_pk_mul_f32 v[66:67], v[66:67], v[84:85]
	v_min_f32_e64 v75, |v68|, s33
	v_min_f32_e64 v73, |v69|, s33
	v_bfi_b32 v68, s2, v75, v68
	v_bfi_b32 v69, s2, v73, v69
	v_cvt_pk_fp8_f32 v72, v68, v69 op_sel:[0,0,1]
	v_min_f32_e64 v68, |v66|, s33
	v_bfi_b32 v66, s2, v68, v66
	v_min_f32_e64 v68, |v67|, s33
	v_bfi_b32 v67, s2, v68, v67
	v_mov_b32_e32 v73, v207
	v_cvt_pk_fp8_f32 v73, v66, v67
	v_min_f32_e64 v68, |v70|, s33
	v_min_f32_e64 v67, |v71|, s33
	v_bfi_b32 v66, s2, v68, v70
	v_bfi_b32 v67, s2, v67, v71
	v_cvt_pk_fp8_f32 v73, v66, v67 op_sel:[0,0,1]
	v_mov_b32_e32 v66, v83
	v_mov_b32_e32 v67, v86
	v_mul_f32_e32 v68, v61, v61
	v_mov_b32_dpp v66, v72 row_ror:8 row_mask:0xf bank_mask:0xc
	v_mov_b32_dpp v67, v73 row_ror:8 row_mask:0xf bank_mask:0xc
	v_mov_b32_dpp v72, v83 row_ror:8 row_mask:0xf bank_mask:0x3
	v_mov_b32_dpp v73, v86 row_ror:8 row_mask:0xf bank_mask:0x3
	global_store_dwordx2 v[114:115], v[66:67], off offset:3072
	global_store_dwordx2 v[114:115], v[72:73], off offset:3584
	v_mul_f32_e32 v66, v63, v63
	v_mul_f32_e32 v67, v65, v65
	v_fmac_f32_e32 v66, v62, v62
	v_fmac_f32_e32 v67, v64, v64
	v_add_f32_e32 v66, v66, v67
	v_mul_f32_e32 v67, v59, v59
	v_fmac_f32_e32 v67, v58, v58
	v_fmac_f32_e32 v68, v60, v60
	v_add_f32_e32 v67, v67, v68
	v_add_f32_e32 v66, v66, v67
	v_mul_f32_e32 v67, v55, v55
	v_mul_f32_e32 v68, v57, v57
	v_fmac_f32_e32 v67, v54, v54
	v_fmac_f32_e32 v68, v56, v56
	v_add_f32_e32 v67, v67, v68
	v_add_f32_e32 v66, v66, v67
	v_mul_f32_e32 v67, v51, v51
	v_mul_f32_e32 v68, v53, v53
	v_fmac_f32_e32 v67, v50, v50
	v_fmac_f32_e32 v68, v52, v52
	v_add_f32_e32 v67, v67, v68
	v_add_f32_e32 v66, v66, v67
	v_mov_b32_e32 v67, v66
	s_nop 1
	v_permlane16_swap_b32_e32 v66, v67
	v_add_f32_e32 v66, v66, v67
	v_mov_b32_e32 v67, v66
	s_nop 1
	v_permlane32_swap_b32_e32 v66, v67
	v_mov_b32_e32 v76, 1.0
	v_mov_b32_e32 v77, 1.0
	v_mov_b32_e32 v80, 1.0
	v_mov_b32_e32 v81, 1.0
	v_mov_b32_e32 v74, 1.0
	v_mov_b32_e32 v75, 1.0
	v_mov_b32_e32 v78, 1.0
	v_mov_b32_e32 v79, 1.0
	s_cbranch_vccnz .LBB0_141
	v_mov_b64_e32 v[68:69], v[156:157]
	v_mov_b64_e32 v[70:71], v[158:159]
	v_mov_b64_e32 v[72:73], v[160:161]
	v_mov_b64_e32 v[74:75], v[162:163]
	v_mov_b32_e32 v78, v130
	v_mov_b32_e32 v79, v130
	v_pk_mul_f32 v[80:81], v[78:79], v[70:71]
	v_pk_mul_f32 v[76:77], v[130:131], v[68:69]
	v_pk_mul_f32 v[78:79], v[78:79], v[74:75]
	v_pk_mul_f32 v[74:75], v[130:131], v[72:73]
.LBB0_141:
	s_and_b64 vcc, exec, s[42:43]
	v_mov_b32_e32 v83, 1.0
	v_mov_b32_e32 v72, 1.0
	v_mov_b32_e32 v73, 1.0
	v_mov_b32_e32 v68, 1.0
	v_mov_b32_e32 v69, 1.0
	v_mov_b32_e32 v70, 1.0
	v_mov_b32_e32 v71, 1.0
	s_cbranch_vccnz .LBB0_143
	v_mov_b64_e32 v[68:69], v[164:165]
	v_mov_b64_e32 v[70:71], v[166:167]
	v_mov_b64_e32 v[84:85], v[168:169]
	v_mov_b64_e32 v[86:87], v[170:171]
	v_mov_b32_e32 v88, v130
	v_mov_b32_e32 v89, v130
	v_pk_mul_f32 v[72:73], v[88:89], v[70:71]
	v_pk_mul_f32 v[82:83], v[130:131], v[68:69]
	v_pk_mul_f32 v[70:71], v[88:89], v[86:87]
	v_pk_mul_f32 v[68:69], v[130:131], v[84:85]
.LBB0_143:
	v_add_f32_e32 v66, v66, v67
	v_fmamk_f32 v66, v66, 0x37800000, v225
	v_mul_f32_e32 v66, 0x3c800000, v66
	v_rsq_f32_e32 v67, v66
	s_addk_i32 s0, 0x80
	v_mov_b32_e32 v66, 1.0
	s_and_b64 vcc, exec, s[42:43]
	v_cndmask_b32_e64 v67, 1.0, v67, s[44:45]
	v_mul_f32_e32 v84, v154, v67
	v_pk_mul_f32 v[62:63], v[62:63], v[84:85] op_sel_hi:[1,0]
	v_pk_mul_f32 v[58:59], v[58:59], v[84:85] op_sel_hi:[1,0]
	v_pk_mul_f32 v[62:63], v[62:63], v[76:77]
	v_pk_mul_f32 v[58:59], v[58:59], v[74:75]
	v_min_f32_e64 v67, |v62|, s33
	v_bfi_b32 v62, s2, v67, v62
	v_min_f32_e64 v67, |v63|, s33
	v_bfi_b32 v63, s2, v67, v63
	v_mov_b32_e32 v74, v207
	v_pk_mul_f32 v[64:65], v[64:65], v[84:85] op_sel_hi:[1,0]
	v_cvt_pk_fp8_f32 v74, v62, v63
	v_pk_mul_f32 v[64:65], v[64:65], v[80:81]
	v_pk_mul_f32 v[60:61], v[60:61], v[84:85] op_sel_hi:[1,0]
	v_min_f32_e64 v67, |v64|, s33
	v_min_f32_e64 v63, |v65|, s33
	v_bfi_b32 v62, s2, v67, v64
	v_bfi_b32 v63, s2, v63, v65
	v_cvt_pk_fp8_f32 v74, v62, v63 op_sel:[0,0,1]
	v_min_f32_e64 v62, |v58|, s33
	v_bfi_b32 v58, s2, v62, v58
	v_min_f32_e64 v62, |v59|, s33
	v_pk_mul_f32 v[60:61], v[60:61], v[78:79]
	v_bfi_b32 v59, s2, v62, v59
	v_mov_b32_e32 v63, v207
	v_pk_mul_f32 v[54:55], v[54:55], v[84:85] op_sel_hi:[1,0]
	v_cvt_pk_fp8_f32 v63, v58, v59
	v_min_f32_e64 v59, |v61|, s33
	v_pk_mul_f32 v[54:55], v[54:55], v[82:83]
	v_bfi_b32 v59, s2, v59, v61
	v_min_f32_e64 v61, |v54|, s33
	v_bfi_b32 v61, s2, v61, v54
	v_min_f32_e64 v54, |v55|, s33
	v_pk_mul_f32 v[56:57], v[56:57], v[84:85] op_sel_hi:[1,0]
	v_bfi_b32 v55, s2, v54, v55
	v_mov_b32_e32 v54, v207
	v_min_f32_e64 v62, |v60|, s33
	v_pk_mul_f32 v[56:57], v[56:57], v[72:73]
	v_cvt_pk_fp8_f32 v54, v61, v55
	v_bfi_b32 v58, s2, v62, v60
	v_min_f32_e64 v62, |v56|, s33
	v_pk_mul_f32 v[50:51], v[50:51], v[84:85] op_sel_hi:[1,0]
	v_bfi_b32 v55, s2, v62, v56
	v_min_f32_e64 v56, |v57|, s33
	v_pk_mul_f32 v[50:51], v[50:51], v[68:69]
	v_bfi_b32 v56, s2, v56, v57
	v_cvt_pk_fp8_f32 v54, v55, v56 op_sel:[0,0,1]
	v_min_f32_e64 v55, |v50|, s33
	v_bfi_b32 v50, s2, v55, v50
	v_min_f32_e64 v55, |v51|, s33
	v_bfi_b32 v51, s2, v55, v51
	v_mov_b32_e32 v55, v207
	v_pk_mul_f32 v[52:53], v[52:53], v[84:85] op_sel_hi:[1,0]
	v_cvt_pk_fp8_f32 v55, v50, v51
	v_pk_mul_f32 v[52:53], v[52:53], v[70:71]
	v_cvt_pk_fp8_f32 v63, v58, v59 op_sel:[0,0,1]
	v_min_f32_e64 v56, |v52|, s33
	v_min_f32_e64 v51, |v53|, s33
	v_bfi_b32 v50, s2, v56, v52
	v_bfi_b32 v51, s2, v51, v53
	v_or_b32_e32 v60, s0, v146
	s_ashr_i32 s0, s0, 12
	v_cvt_pk_fp8_f32 v55, v50, v51 op_sel:[0,0,1]
	s_ashr_i32 s1, s0, 31
	s_lshl_b64 s[0:1], s[0:1], 21
	v_lshlrev_b32_e32 v50, 6, v60
	v_lshl_add_u64 v[58:59], v[122:123], 0, s[0:1]
	v_mov_b32_e32 v52, v74
	v_mov_b32_e32 v53, v63
	v_and_b32_e32 v206, 0x3f1c0, v50
	v_mov_b32_dpp v52, v54 row_ror:8 row_mask:0xf bank_mask:0xc
	v_mov_b32_dpp v53, v55 row_ror:8 row_mask:0xf bank_mask:0xc
	v_lshl_add_u64 v[50:51], v[58:59], 0, v[206:207]
	v_mov_b32_dpp v54, v74 row_ror:8 row_mask:0xf bank_mask:0x3
	v_mov_b32_dpp v55, v63 row_ror:8 row_mask:0xf bank_mask:0x3
	global_store_dwordx2 v[50:51], v[52:53], off
	global_store_dwordx2 v[50:51], v[54:55], off offset:512
	v_mul_f32_e32 v52, v47, v47
	v_mul_f32_e32 v53, v49, v49
	v_fmac_f32_e32 v52, v46, v46
	v_fmac_f32_e32 v53, v48, v48
	v_add_f32_e32 v52, v52, v53
	v_mul_f32_e32 v53, v43, v43
	v_mul_f32_e32 v54, v45, v45
	v_fmac_f32_e32 v53, v42, v42
	v_fmac_f32_e32 v54, v44, v44
	v_add_f32_e32 v53, v53, v54
	v_add_f32_e32 v52, v52, v53
	v_mul_f32_e32 v53, v39, v39
	v_mul_f32_e32 v54, v41, v41
	v_fmac_f32_e32 v53, v38, v38
	v_fmac_f32_e32 v54, v40, v40
	v_add_f32_e32 v53, v53, v54
	v_add_f32_e32 v52, v52, v53
	v_mul_f32_e32 v53, v35, v35
	v_mul_f32_e32 v54, v37, v37
	v_fmac_f32_e32 v53, v34, v34
	v_fmac_f32_e32 v54, v36, v36
	v_add_f32_e32 v53, v53, v54
	v_add_f32_e32 v52, v52, v53
	v_mov_b32_e32 v53, v52
	s_nop 1
	v_permlane16_swap_b32_e32 v52, v53
	v_add_f32_e32 v52, v52, v53
	v_mov_b32_e32 v53, v52
	s_nop 1
	v_permlane32_swap_b32_e32 v52, v53
	v_mov_b32_e32 v58, 1.0
	v_mov_b32_e32 v59, 1.0
	v_mov_b32_e32 v68, 1.0
	v_mov_b32_e32 v69, 1.0
	v_mov_b32_e32 v56, 1.0
	v_mov_b32_e32 v57, 1.0
	v_mov_b32_e32 v62, 1.0
	v_mov_b32_e32 v63, 1.0
	s_cbranch_vccnz .LBB0_145
	v_mov_b64_e32 v[54:55], v[156:157]
	v_mov_b64_e32 v[56:57], v[158:159]
	v_mov_b64_e32 v[60:61], v[160:161]
	v_mov_b64_e32 v[62:63], v[162:163]
	v_mov_b32_e32 v64, v130
	v_mov_b32_e32 v65, v130
	v_pk_mul_f32 v[68:69], v[64:65], v[56:57]
	v_pk_mul_f32 v[58:59], v[130:131], v[54:55]
	v_pk_mul_f32 v[62:63], v[64:65], v[62:63]
	v_pk_mul_f32 v[56:57], v[130:131], v[60:61]
.LBB0_145:
	s_and_b64 vcc, exec, s[42:43]
	v_mov_b32_e32 v67, 1.0
	v_mov_b32_e32 v64, 1.0
	v_mov_b32_e32 v65, 1.0
	v_mov_b32_e32 v54, 1.0
	v_mov_b32_e32 v55, 1.0
	v_mov_b32_e32 v60, 1.0
	v_mov_b32_e32 v61, 1.0
	s_cbranch_vccnz .LBB0_147
	v_mov_b64_e32 v[70:71], v[164:165]
	v_mov_b64_e32 v[72:73], v[166:167]
	v_mov_b64_e32 v[74:75], v[168:169]
	v_mov_b64_e32 v[76:77], v[170:171]
	v_mov_b32_e32 v54, v130
	v_mov_b32_e32 v55, v130
	v_pk_mul_f32 v[64:65], v[54:55], v[72:73]
	v_pk_mul_f32 v[66:67], v[130:131], v[70:71]
	v_pk_mul_f32 v[60:61], v[54:55], v[76:77]
	v_pk_mul_f32 v[54:55], v[130:131], v[74:75]
.LBB0_147:
	v_add_f32_e32 v52, v52, v53
	v_fmamk_f32 v52, v52, 0x37800000, v225
	v_mul_f32_e32 v52, 0x3c800000, v52
	v_rsq_f32_e32 v53, v52
	v_mov_b32_e32 v52, 1.0
	s_and_b64 vcc, exec, s[42:43]
	v_cndmask_b32_e64 v53, 1.0, v53, s[44:45]
	v_mul_f32_e32 v70, v154, v53
	v_pk_mul_f32 v[46:47], v[46:47], v[70:71] op_sel_hi:[1,0]
	v_pk_mul_f32 v[42:43], v[42:43], v[70:71] op_sel_hi:[1,0]
	v_pk_mul_f32 v[46:47], v[46:47], v[58:59]
	v_pk_mul_f32 v[42:43], v[42:43], v[56:57]
	v_min_f32_e64 v53, |v46|, s33
	v_bfi_b32 v46, s2, v53, v46
	v_min_f32_e64 v53, |v47|, s33
	v_bfi_b32 v47, s2, v53, v47
	v_mov_b32_e32 v56, v207
	v_pk_mul_f32 v[48:49], v[48:49], v[70:71] op_sel_hi:[1,0]
	v_cvt_pk_fp8_f32 v56, v46, v47
	v_pk_mul_f32 v[48:49], v[48:49], v[68:69]
	v_pk_mul_f32 v[44:45], v[44:45], v[70:71] op_sel_hi:[1,0]
	v_min_f32_e64 v53, |v48|, s33
	v_min_f32_e64 v47, |v49|, s33
	v_bfi_b32 v46, s2, v53, v48
	v_bfi_b32 v47, s2, v47, v49
	v_cvt_pk_fp8_f32 v56, v46, v47 op_sel:[0,0,1]
	v_min_f32_e64 v46, |v42|, s33
	v_bfi_b32 v42, s2, v46, v42
	v_min_f32_e64 v46, |v43|, s33
	v_bfi_b32 v43, s2, v46, v43
	v_mov_b32_e32 v47, v207
	v_cvt_pk_fp8_f32 v47, v42, v43
	v_pk_mul_f32 v[44:45], v[44:45], v[62:63]
	v_pk_mul_f32 v[38:39], v[38:39], v[70:71] op_sel_hi:[1,0]
	v_min_f32_e64 v46, |v44|, s33
	v_min_f32_e64 v43, |v45|, s33
	v_bfi_b32 v42, s2, v46, v44
	v_bfi_b32 v43, s2, v43, v45
	v_pk_mul_f32 v[38:39], v[38:39], v[66:67]
	v_cvt_pk_fp8_f32 v47, v42, v43 op_sel:[0,0,1]
	v_min_f32_e64 v42, |v38|, s33
	v_bfi_b32 v42, s2, v42, v38
	v_min_f32_e64 v38, |v39|, s33
	v_pk_mul_f32 v[40:41], v[40:41], v[70:71] op_sel_hi:[1,0]
	v_bfi_b32 v39, s2, v38, v39
	v_mov_b32_e32 v38, v207
	v_pk_mul_f32 v[40:41], v[40:41], v[64:65]
	v_cvt_pk_fp8_f32 v38, v42, v39
	v_min_f32_e64 v43, |v40|, s33
	v_pk_mul_f32 v[34:35], v[34:35], v[70:71] op_sel_hi:[1,0]
	v_bfi_b32 v39, s2, v43, v40
	v_min_f32_e64 v40, |v41|, s33
	v_pk_mul_f32 v[34:35], v[34:35], v[54:55]
	v_bfi_b32 v40, s2, v40, v41
	v_cvt_pk_fp8_f32 v38, v39, v40 op_sel:[0,0,1]
	v_min_f32_e64 v39, |v34|, s33
	v_bfi_b32 v34, s2, v39, v34
	v_min_f32_e64 v39, |v35|, s33
	v_bfi_b32 v35, s2, v39, v35
	v_mov_b32_e32 v39, v207
	v_pk_mul_f32 v[36:37], v[36:37], v[70:71] op_sel_hi:[1,0]
	v_cvt_pk_fp8_f32 v39, v34, v35
	v_pk_mul_f32 v[36:37], v[36:37], v[60:61]
	v_mov_b32_e32 v46, 1.0
	v_min_f32_e64 v40, |v36|, s33
	v_min_f32_e64 v35, |v37|, s33
	v_bfi_b32 v34, s2, v40, v36
	v_bfi_b32 v35, s2, v35, v37
	v_cvt_pk_fp8_f32 v39, v34, v35 op_sel:[0,0,1]
	v_mov_b32_e32 v34, v56
	v_mov_b32_e32 v35, v47
	v_mul_f32_e32 v36, v29, v29
	v_mov_b32_dpp v34, v38 row_ror:8 row_mask:0xf bank_mask:0xc
	v_mov_b32_dpp v35, v39 row_ror:8 row_mask:0xf bank_mask:0xc
	v_mov_b32_dpp v38, v56 row_ror:8 row_mask:0xf bank_mask:0x3
	v_mov_b32_dpp v39, v47 row_ror:8 row_mask:0xf bank_mask:0x3
	global_store_dwordx2 v[50:51], v[34:35], off offset:1024
	global_store_dwordx2 v[50:51], v[38:39], off offset:1536
	v_mul_f32_e32 v34, v31, v31
	v_mul_f32_e32 v35, v33, v33
	v_fmac_f32_e32 v34, v30, v30
	v_fmac_f32_e32 v35, v32, v32
	v_add_f32_e32 v34, v34, v35
	v_mul_f32_e32 v35, v27, v27
	v_fmac_f32_e32 v35, v26, v26
	v_fmac_f32_e32 v36, v28, v28
	v_add_f32_e32 v35, v35, v36
	v_add_f32_e32 v34, v34, v35
	v_mul_f32_e32 v35, v23, v23
	v_mul_f32_e32 v36, v25, v25
	v_fmac_f32_e32 v35, v22, v22
	v_fmac_f32_e32 v36, v24, v24
	v_add_f32_e32 v35, v35, v36
	v_add_f32_e32 v34, v34, v35
	v_mul_f32_e32 v35, v19, v19
	v_mul_f32_e32 v36, v21, v21
	v_fmac_f32_e32 v35, v18, v18
	v_fmac_f32_e32 v36, v20, v20
	v_add_f32_e32 v35, v35, v36
	v_add_f32_e32 v34, v34, v35
	v_mov_b32_e32 v35, v34
	s_nop 1
	v_permlane16_swap_b32_e32 v34, v35
	v_add_f32_e32 v48, v34, v35
	v_mov_b32_e32 v49, v48
	s_nop 1
	v_permlane32_swap_b32_e32 v48, v49
	v_mov_b32_e32 v38, 1.0
	v_mov_b32_e32 v39, 1.0
	v_mov_b32_e32 v47, 1.0
	v_mov_b32_e32 v36, 1.0
	v_mov_b32_e32 v37, 1.0
	v_mov_b32_e32 v42, 1.0
	v_mov_b32_e32 v43, 1.0
	s_cbranch_vccnz .LBB0_149
	v_mov_b64_e32 v[34:35], v[156:157]
	v_mov_b64_e32 v[36:37], v[158:159]
	v_mov_b64_e32 v[40:41], v[160:161]
	v_mov_b64_e32 v[42:43], v[162:163]
	v_mov_b32_e32 v44, v130
	v_mov_b32_e32 v45, v130
	v_pk_mul_f32 v[46:47], v[44:45], v[36:37]
	v_pk_mul_f32 v[38:39], v[130:131], v[34:35]
	v_pk_mul_f32 v[42:43], v[44:45], v[42:43]
	v_pk_mul_f32 v[36:37], v[130:131], v[40:41]
.LBB0_149:
	s_and_b64 vcc, exec, s[42:43]
	v_mov_b32_e32 v53, 1.0
	v_mov_b32_e32 v44, 1.0
	v_mov_b32_e32 v45, 1.0
	v_mov_b32_e32 v34, 1.0
	v_mov_b32_e32 v35, 1.0
	v_mov_b32_e32 v40, 1.0
	v_mov_b32_e32 v41, 1.0
	s_cbranch_vccnz .LBB0_151
	v_mov_b64_e32 v[52:53], v[164:165]
	v_mov_b64_e32 v[54:55], v[166:167]
	v_mov_b64_e32 v[56:57], v[168:169]
	v_mov_b64_e32 v[58:59], v[170:171]
	v_mov_b32_e32 v34, v130
	v_mov_b32_e32 v35, v130
	v_pk_mul_f32 v[44:45], v[34:35], v[54:55]
	v_pk_mul_f32 v[52:53], v[130:131], v[52:53]
	v_pk_mul_f32 v[40:41], v[34:35], v[58:59]
	v_pk_mul_f32 v[34:35], v[130:131], v[56:57]
.LBB0_151:
	v_add_f32_e32 v48, v48, v49
	v_fmamk_f32 v48, v48, 0x37800000, v225
	v_mul_f32_e32 v48, 0x3c800000, v48
	v_rsq_f32_e32 v49, v48
	v_mov_b32_e32 v48, 1.0
	s_and_b64 vcc, exec, s[42:43]
	v_cndmask_b32_e64 v49, 1.0, v49, s[44:45]
	v_mul_f32_e32 v54, v154, v49
	v_pk_mul_f32 v[30:31], v[30:31], v[54:55] op_sel_hi:[1,0]
	v_pk_mul_f32 v[26:27], v[26:27], v[54:55] op_sel_hi:[1,0]
	v_pk_mul_f32 v[30:31], v[30:31], v[38:39]
	v_pk_mul_f32 v[26:27], v[26:27], v[36:37]
	v_min_f32_e64 v36, |v30|, s33
	v_bfi_b32 v30, s2, v36, v30
	v_min_f32_e64 v36, |v31|, s33
	v_bfi_b32 v31, s2, v36, v31
	v_mov_b32_e32 v37, v207
	v_pk_mul_f32 v[32:33], v[32:33], v[54:55] op_sel_hi:[1,0]
	v_cvt_pk_fp8_f32 v37, v30, v31
	v_pk_mul_f32 v[32:33], v[32:33], v[46:47]
	v_pk_mul_f32 v[28:29], v[28:29], v[54:55] op_sel_hi:[1,0]
	v_min_f32_e64 v36, |v32|, s33
	v_min_f32_e64 v31, |v33|, s33
	v_bfi_b32 v30, s2, v36, v32
	v_bfi_b32 v31, s2, v31, v33
	v_cvt_pk_fp8_f32 v37, v30, v31 op_sel:[0,0,1]
	v_min_f32_e64 v30, |v26|, s33
	v_bfi_b32 v26, s2, v30, v26
	v_min_f32_e64 v30, |v27|, s33
	v_bfi_b32 v27, s2, v30, v27
	v_mov_b32_e32 v31, v207
	v_cvt_pk_fp8_f32 v31, v26, v27
	v_pk_mul_f32 v[28:29], v[28:29], v[42:43]
	v_pk_mul_f32 v[22:23], v[22:23], v[54:55] op_sel_hi:[1,0]
	v_min_f32_e64 v30, |v28|, s33
	v_min_f32_e64 v27, |v29|, s33
	v_bfi_b32 v26, s2, v30, v28
	v_bfi_b32 v27, s2, v27, v29
	v_pk_mul_f32 v[22:23], v[22:23], v[52:53]
	v_cvt_pk_fp8_f32 v31, v26, v27 op_sel:[0,0,1]
	v_min_f32_e64 v26, |v22|, s33
	v_bfi_b32 v26, s2, v26, v22
	v_min_f32_e64 v22, |v23|, s33
	v_pk_mul_f32 v[24:25], v[24:25], v[54:55] op_sel_hi:[1,0]
	v_bfi_b32 v23, s2, v22, v23
	v_mov_b32_e32 v22, v207
	v_pk_mul_f32 v[24:25], v[24:25], v[44:45]
	v_cvt_pk_fp8_f32 v22, v26, v23
	v_min_f32_e64 v27, |v24|, s33
	v_pk_mul_f32 v[18:19], v[18:19], v[54:55] op_sel_hi:[1,0]
	v_bfi_b32 v23, s2, v27, v24
	v_min_f32_e64 v24, |v25|, s33
	v_pk_mul_f32 v[18:19], v[18:19], v[34:35]
	v_bfi_b32 v24, s2, v24, v25
	v_cvt_pk_fp8_f32 v22, v23, v24 op_sel:[0,0,1]
	v_min_f32_e64 v23, |v18|, s33
	v_bfi_b32 v18, s2, v23, v18
	v_min_f32_e64 v23, |v19|, s33
	v_bfi_b32 v19, s2, v23, v19
	v_mov_b32_e32 v23, v207
	v_pk_mul_f32 v[20:21], v[20:21], v[54:55] op_sel_hi:[1,0]
	v_cvt_pk_fp8_f32 v23, v18, v19
	v_pk_mul_f32 v[20:21], v[20:21], v[40:41]
	v_mov_b32_e32 v30, 1.0
	v_min_f32_e64 v24, |v20|, s33
	v_min_f32_e64 v19, |v21|, s33
	v_bfi_b32 v18, s2, v24, v20
	v_bfi_b32 v19, s2, v19, v21
	v_cvt_pk_fp8_f32 v23, v18, v19 op_sel:[0,0,1]
	v_mov_b32_e32 v18, v37
	v_mov_b32_e32 v19, v31
	v_mul_f32_e32 v20, v17, v17
	v_mov_b32_dpp v18, v22 row_ror:8 row_mask:0xf bank_mask:0xc
	v_mov_b32_dpp v19, v23 row_ror:8 row_mask:0xf bank_mask:0xc
	v_mov_b32_dpp v22, v37 row_ror:8 row_mask:0xf bank_mask:0x3
	v_mov_b32_dpp v23, v31 row_ror:8 row_mask:0xf bank_mask:0x3
	global_store_dwordx2 v[50:51], v[18:19], off offset:2048
	global_store_dwordx2 v[50:51], v[22:23], off offset:2560
	v_mul_f32_e32 v18, v3, v3
	v_mul_f32_e32 v19, v5, v5
	v_fmac_f32_e32 v18, v2, v2
	v_fmac_f32_e32 v19, v4, v4
	v_add_f32_e32 v18, v18, v19
	v_mul_f32_e32 v19, v15, v15
	v_fmac_f32_e32 v19, v14, v14
	v_fmac_f32_e32 v20, v16, v16
	v_add_f32_e32 v19, v19, v20
	v_add_f32_e32 v18, v18, v19
	v_mul_f32_e32 v19, v11, v11
	v_mul_f32_e32 v20, v13, v13
	v_fmac_f32_e32 v19, v10, v10
	v_fmac_f32_e32 v20, v12, v12
	v_add_f32_e32 v19, v19, v20
	v_add_f32_e32 v18, v18, v19
	v_mul_f32_e32 v19, v7, v7
	v_mul_f32_e32 v20, v9, v9
	v_fmac_f32_e32 v19, v6, v6
	v_fmac_f32_e32 v20, v8, v8
	v_add_f32_e32 v19, v19, v20
	v_add_f32_e32 v18, v18, v19
	v_mov_b32_e32 v19, v18
	s_nop 1
	v_permlane16_swap_b32_e32 v18, v19
	v_add_f32_e32 v34, v18, v19
	v_mov_b32_e32 v35, v34
	s_nop 1
	v_permlane32_swap_b32_e32 v34, v35
	v_mov_b32_e32 v20, 1.0
	v_mov_b32_e32 v21, 1.0
	v_mov_b32_e32 v18, 1.0
	v_mov_b32_e32 v19, 1.0
	v_mov_b32_e32 v31, 1.0
	v_mov_b32_e32 v26, 1.0
	v_mov_b32_e32 v27, 1.0
	s_cbranch_vccnz .LBB0_153
	v_mov_b64_e32 v[20:21], v[156:157]
	v_mov_b64_e32 v[22:23], v[158:159]
	v_mov_b64_e32 v[24:25], v[160:161]
	v_mov_b64_e32 v[26:27], v[162:163]
	v_mov_b32_e32 v28, v130
	v_mov_b32_e32 v29, v130
	v_pk_mul_f32 v[18:19], v[28:29], v[22:23]
	v_pk_mul_f32 v[20:21], v[130:131], v[20:21]
	v_pk_mul_f32 v[26:27], v[28:29], v[26:27]
	v_pk_mul_f32 v[30:31], v[130:131], v[24:25]
.LBB0_153:
	s_and_b64 vcc, exec, s[42:43]
	v_mov_b32_e32 v24, 1.0
	v_mov_b32_e32 v25, 1.0
	v_mov_b32_e32 v32, 1.0
	v_mov_b32_e32 v33, 1.0
	v_mov_b32_e32 v22, 1.0
	v_mov_b32_e32 v23, 1.0
	v_mov_b32_e32 v28, 1.0
	v_mov_b32_e32 v29, 1.0
	s_cbranch_vccnz .LBB0_155
	v_mov_b64_e32 v[22:23], v[164:165]
	v_mov_b64_e32 v[24:25], v[166:167]
	v_mov_b64_e32 v[36:37], v[168:169]
	v_mov_b64_e32 v[38:39], v[170:171]
	v_add_f32_e32 v32, v34, v35
	v_fmamk_f32 v32, v32, 0x37800000, v225
	v_mul_f32_e32 v32, 0x3c800000, v32
	v_rsq_f32_e32 v48, v32
	v_mov_b32_e32 v28, v130
	v_mov_b32_e32 v29, v130
	v_pk_mul_f32 v[32:33], v[28:29], v[24:25]
	v_pk_mul_f32 v[24:25], v[130:131], v[22:23]
	v_pk_mul_f32 v[28:29], v[28:29], v[38:39]
	v_pk_mul_f32 v[22:23], v[130:131], v[36:37]
